# removed 111 redundant zero-inits (v_mov vX, 0) ahead of v_cvt_pk_fp8_f32 low/high pairs in the fp8 epilogues and norm phases (on top of v54)
# speedup vs baseline: 1.0075x; 1.0034x over previous
.LBB0_373:
	v_cvt_pk_fp8_f32 v76, v74, v75
	v_cvt_pk_fp8_f32 v76, v72, v73 op_sel:[0,0,1]
	global_store_dword v[78:79], v76, off offset:768

.LBB0_407:
	v_cvt_pk_fp8_f32 v104, v100, v101
	v_lshl_add_u64 v[100:101], s[60:61], 0, v[182:183]
	v_mov_b32_e32 v169, v168
	v_readlane_b32 s2, v252, 1
	v_cvt_pk_fp8_f32 v104, v102, v103 op_sel:[0,0,1]
	v_add_co_u32_e32 v102, vcc, 0x6a265000, v100
	v_pk_add_f32 v[94:95], v[94:95], 1.0 op_sel_hi:[1,0]
	s_nop 0
	v_addc_co_u32_e32 v103, vcc, 0, v101, vcc
	global_store_dword v[102:103], v104, off offset:1536
	v_cvt_pk_bf16_f32 v102, v152, v153
	v_cvt_pk_bf16_f32 v103, v154, v155
	global_store_dwordx2 v[170:171], v[102:103], off offset:512
	v_mov_b32_e32 v102, v168
	v_mov_b32_e32 v103, v168
	v_pk_mul_f32 v[102:103], v[154:155], v[102:103]
	v_pk_mul_f32 v[104:105], v[152:153], v[168:169]
	v_pk_mul_f32 v[102:103], v[6:7], v[102:103]
	v_readlane_b32 s3, v252, 2
	v_pk_mul_f32 v[104:105], v[4:5], v[104:105]
	v_pk_add_f32 v[92:93], v[92:93], 1.0 op_sel_hi:[1,0]
	v_pk_fma_f32 v[90:91], v[94:95], v[102:103], v[90:91]
	v_cndmask_b32_e64 v94, 0, 1, s[2:3]
	v_pk_fma_f32 v[88:89], v[92:93], v[104:105], v[88:89]
	v_cmp_ne_u32_e64 s[6:7], 1, v94
	s_andn2_b64 vcc, exec, s[2:3]
	s_mov_b64 s[2:3], -1
	v_cvt_pk_bf16_f32 v92, v88, v89
	v_cvt_pk_bf16_f32 v93, v90, v91
	s_cbranch_vccnz .LBB0_409
	v_add_co_u32_e32 v94, vcc, 0x3f538000, v186
	s_mov_b64 s[2:3], 0
	s_nop 0
	v_addc_co_u32_e32 v95, vcc, 0, v187, vcc
	global_store_dwordx2 v[94:95], v[92:93], off offset:512

.LBB0_411:
	v_cvt_pk_fp8_f32 v92, v88, v89
	v_add_co_u32_e32 v88, vcc, 0x6a265000, v100
	v_pk_add_f32 v[86:87], v[86:87], 1.0 op_sel_hi:[1,0]
	v_cvt_pk_fp8_f32 v92, v90, v91 op_sel:[0,0,1]
	v_addc_co_u32_e32 v89, vcc, 0, v101, vcc
	v_pk_mul_f32 v[90:91], v[140:141], v[168:169]
	global_store_dword v[88:89], v92, off offset:1792
	v_cvt_pk_bf16_f32 v88, v140, v141
	v_cvt_pk_bf16_f32 v89, v142, v143
	global_store_dwordx2 v[170:171], v[88:89], off offset:1024
	v_mov_b32_e32 v88, v168
	v_mov_b32_e32 v89, v168
	v_pk_mul_f32 v[88:89], v[142:143], v[88:89]
	v_pk_mul_f32 v[90:91], v[8:9], v[90:91]
	v_pk_mul_f32 v[88:89], v[10:11], v[88:89]
	v_pk_add_f32 v[84:85], v[84:85], 1.0 op_sel_hi:[1,0]
	v_pk_fma_f32 v[82:83], v[86:87], v[88:89], v[82:83]
	v_pk_fma_f32 v[80:81], v[84:85], v[90:91], v[80:81]
	s_mov_b64 s[2:3], -1
	s_and_b64 vcc, exec, s[6:7]
	v_cvt_pk_bf16_f32 v84, v80, v81
	v_cvt_pk_bf16_f32 v85, v82, v83
	s_cbranch_vccnz .LBB0_413
	v_add_co_u32_e32 v86, vcc, 0x3f538000, v186
	s_mov_b64 s[2:3], 0
	s_nop 0
	v_addc_co_u32_e32 v87, vcc, 0, v187, vcc
	global_store_dwordx2 v[86:87], v[84:85], off offset:1024

.LBB0_415:
	v_cvt_pk_fp8_f32 v84, v80, v81
	v_add_co_u32_e32 v80, vcc, 0x6a265000, v100
	v_pk_add_f32 v[78:79], v[78:79], 1.0 op_sel_hi:[1,0]
	v_cvt_pk_fp8_f32 v84, v82, v83 op_sel:[0,0,1]
	v_addc_co_u32_e32 v81, vcc, 0, v101, vcc
	v_pk_mul_f32 v[82:83], v[144:145], v[168:169]
	global_store_dword v[80:81], v84, off offset:2048
	v_cvt_pk_bf16_f32 v80, v144, v145
	v_cvt_pk_bf16_f32 v81, v146, v147
	global_store_dwordx2 v[170:171], v[80:81], off offset:1536
	v_mov_b32_e32 v80, v168
	v_mov_b32_e32 v81, v168
	v_pk_mul_f32 v[80:81], v[146:147], v[80:81]
	v_pk_mul_f32 v[82:83], v[12:13], v[82:83]
	v_pk_mul_f32 v[80:81], v[14:15], v[80:81]
	v_pk_add_f32 v[76:77], v[76:77], 1.0 op_sel_hi:[1,0]
	v_pk_fma_f32 v[74:75], v[78:79], v[80:81], v[74:75]
	v_pk_fma_f32 v[72:73], v[76:77], v[82:83], v[72:73]
	s_mov_b64 s[2:3], -1
	s_and_b64 vcc, exec, s[6:7]
	v_cvt_pk_bf16_f32 v76, v72, v73
	v_cvt_pk_bf16_f32 v77, v74, v75
	s_cbranch_vccnz .LBB0_417
	v_add_co_u32_e32 v78, vcc, 0x3f538000, v186
	s_mov_b64 s[2:3], 0
	s_nop 0
	v_addc_co_u32_e32 v79, vcc, 0, v187, vcc
	global_store_dwordx2 v[78:79], v[76:77], off offset:1536

.LBB0_419:
	v_cvt_pk_fp8_f32 v76, v72, v73
	v_add_co_u32_e32 v72, vcc, 0x6a265000, v100
	v_mul_f32_e32 v77, v165, v165
	v_cvt_pk_fp8_f32 v76, v74, v75 op_sel:[0,0,1]
	v_addc_co_u32_e32 v73, vcc, 0, v101, vcc
	v_mul_f32_e32 v74, v159, v159
	global_store_dword v[72:73], v76, off offset:2304
	v_mul_f32_e32 v72, v167, v167
	v_mul_f32_e32 v73, v157, v157
	v_fmac_f32_e32 v77, v164, v164
	v_fmac_f32_e32 v72, v166, v166
	v_fmac_f32_e32 v73, v156, v156
	v_fmac_f32_e32 v74, v158, v158
	v_add_f32_e32 v72, v77, v72
	v_add_f32_e32 v73, v73, v74
	v_add_f32_e32 v72, v72, v73
	v_mul_f32_e32 v73, v149, v149
	v_mul_f32_e32 v74, v151, v151
	v_fmac_f32_e32 v73, v148, v148
	v_fmac_f32_e32 v74, v150, v150
	v_add_f32_e32 v73, v73, v74
	v_add_f32_e32 v72, v72, v73
	v_mul_f32_e32 v73, v97, v97
	v_mul_f32_e32 v74, v99, v99
	v_fmac_f32_e32 v73, v96, v96
	v_fmac_f32_e32 v74, v98, v98
	v_add_f32_e32 v73, v73, v74
	v_add_f32_e32 v72, v72, v73
	v_mov_b32_e32 v73, v173
	s_andn2_b64 vcc, exec, s[22:23]
	v_add_f32_dpp v72, v72, v72 quad_perm:[1,0,3,2] row_mask:0xf bank_mask:0xf bound_ctrl:1
	s_nop 1
	v_add_f32_dpp v72, v72, v72 quad_perm:[2,3,0,1] row_mask:0xf bank_mask:0xf bound_ctrl:1
	s_nop 1
	v_add_f32_dpp v72, v72, v72 row_half_mirror row_mask:0xf bank_mask:0xf bound_ctrl:1
	s_nop 1
	v_add_f32_dpp v72, v72, v72 row_mirror row_mask:0xf bank_mask:0xf bound_ctrl:1
	s_nop 1
	v_mov_b32_dpp v73, v72 row_bcast:15 row_mask:0xa bank_mask:0xf
	v_add_f32_e32 v72, v72, v73
	v_mov_b32_e32 v73, v173
	s_nop 1
	v_mov_b32_dpp v73, v72 row_bcast:31 row_mask:0xc bank_mask:0xf
	v_add_f32_e32 v72, v72, v73
	s_nop 0
	v_readlane_b32 s2, v72, 63
	s_cbranch_vccnz .LBB0_374
	s_nop 0
	v_fma_f32 v72, s2, v212, v198
	v_mul_f32_e32 v73, 0x4b800000, v72
	v_cmp_gt_f32_e32 vcc, s0, v72
	s_ashr_i32 s21, s20, 31
	s_lshl_b64 s[2:3], s[20:21], 11
	v_cndmask_b32_e32 v72, v72, v73, vcc
	v_rsq_f32_e32 v72, v72
	v_readlane_b32 s0, v250, 13
	v_cvt_pk_bf16_f32 v76, v164, v165
	v_cvt_pk_bf16_f32 v77, v166, v167
	v_mul_f32_e32 v73, 0x45800000, v72
	v_cndmask_b32_e32 v72, v72, v73, vcc
	v_lshl_add_u64 v[74:75], v[178:179], 0, s[2:3]
	s_add_u32 s16, s0, s2
	v_readlane_b32 s0, v250, 14
	global_store_dwordx2 v[74:75], v[76:77], off
	v_pk_mul_f32 v[76:77], v[166:167], v[72:73] op_sel_hi:[1,0]
	v_pk_mul_f32 v[78:79], v[164:165], v[72:73] op_sel_hi:[1,0]
	s_addc_u32 s17, s0, s3
	v_pk_mul_f32 v[80:81], v[0:1], v[78:79]
	v_pk_mul_f32 v[76:77], v[2:3], v[76:77]
	v_pk_add_f32 v[78:79], v[138:139], 1.0 op_sel_hi:[1,0]
	v_pk_add_f32 v[82:83], v[136:137], 1.0 op_sel_hi:[1,0]
	v_pk_fma_f32 v[78:79], v[78:79], v[76:77], v[134:135]
	v_pk_fma_f32 v[80:81], v[82:83], v[80:81], v[132:133]
	s_mov_b64 s[2:3], -1
	s_and_b64 vcc, exec, s[6:7]
	v_lshl_add_u64 v[76:77], v[174:175], 1, s[16:17]
	v_cvt_pk_bf16_f32 v82, v80, v81
	v_cvt_pk_bf16_f32 v83, v78, v79
	s_cbranch_vccnz .LBB0_422
	s_mov_b64 s[2:3], 0
	global_store_dwordx2 v[76:77], v[82:83], off

.LBB0_424:
	v_cvt_pk_fp8_f32 v82, v80, v81
	s_lshl_b64 s[2:3], s[20:21], 10
	v_cvt_pk_bf16_f32 v80, v156, v157
	v_cvt_pk_bf16_f32 v81, v158, v159
	v_cvt_pk_fp8_f32 v82, v78, v79 op_sel:[0,0,1]
	v_lshl_add_u64 v[78:79], v[180:181], 0, s[2:3]
	v_mov_b32_e32 v73, v72
	v_pk_add_f32 v[84:85], v[130:131], 1.0 op_sel_hi:[1,0]
	global_store_dword v[78:79], v82, off
	global_store_dwordx2 v[74:75], v[80:81], off offset:512
	v_mov_b32_e32 v80, v72
	v_mov_b32_e32 v81, v72
	v_pk_mul_f32 v[80:81], v[158:159], v[80:81]
	v_pk_mul_f32 v[82:83], v[156:157], v[72:73]
	v_pk_mul_f32 v[80:81], v[6:7], v[80:81]
	v_pk_mul_f32 v[82:83], v[4:5], v[82:83]
	v_pk_add_f32 v[86:87], v[128:129], 1.0 op_sel_hi:[1,0]
	v_pk_fma_f32 v[80:81], v[84:85], v[80:81], v[126:127]
	v_pk_fma_f32 v[82:83], v[86:87], v[82:83], v[124:125]
	s_and_b64 vcc, exec, s[6:7]
	s_mov_b64 s[2:3], -1
	v_cvt_pk_bf16_f32 v84, v82, v83
	v_cvt_pk_bf16_f32 v85, v80, v81
	s_cbranch_vccnz .LBB0_426
	s_mov_b64 s[2:3], 0
	global_store_dwordx2 v[76:77], v[84:85], off offset:512

.LBB0_428:
	v_cvt_pk_fp8_f32 v84, v82, v83
	v_pk_mul_f32 v[82:83], v[148:149], v[72:73]
	v_pk_add_f32 v[86:87], v[120:121], 1.0 op_sel_hi:[1,0]
	v_pk_mul_f32 v[82:83], v[8:9], v[82:83]
	v_cvt_pk_fp8_f32 v84, v80, v81 op_sel:[0,0,1]
	v_cvt_pk_bf16_f32 v80, v148, v149
	v_cvt_pk_bf16_f32 v81, v150, v151
	v_pk_fma_f32 v[82:83], v[86:87], v[82:83], v[116:117]
	global_store_dword v[78:79], v84, off offset:256
	global_store_dwordx2 v[74:75], v[80:81], off offset:1024
	v_mov_b32_e32 v80, v72
	v_mov_b32_e32 v81, v72
	v_pk_mul_f32 v[80:81], v[150:151], v[80:81]
	v_pk_add_f32 v[84:85], v[122:123], 1.0 op_sel_hi:[1,0]
	v_pk_mul_f32 v[80:81], v[10:11], v[80:81]
	s_mov_b64 s[2:3], -1
	v_pk_fma_f32 v[80:81], v[84:85], v[80:81], v[118:119]
	s_and_b64 vcc, exec, s[6:7]
	v_cvt_pk_bf16_f32 v84, v82, v83
	v_cvt_pk_bf16_f32 v85, v80, v81
	s_cbranch_vccnz .LBB0_430
	s_mov_b64 s[2:3], 0
	global_store_dwordx2 v[76:77], v[84:85], off offset:1024

.LBB0_432:
	v_cvt_pk_fp8_f32 v84, v82, v83
	v_cvt_pk_bf16_f32 v82, v96, v97
	v_cvt_pk_bf16_f32 v83, v98, v99
	s_and_b64 vcc, exec, s[6:7]
	v_cvt_pk_fp8_f32 v84, v80, v81 op_sel:[0,0,1]
	v_mov_b32_e32 v80, v72
	v_mov_b32_e32 v81, v72
	v_pk_mul_f32 v[80:81], v[98:99], v[80:81]
	v_pk_mul_f32 v[72:73], v[96:97], v[72:73]
	global_store_dword v[78:79], v84, off offset:512
	global_store_dwordx2 v[74:75], v[82:83], off offset:1536
	v_pk_mul_f32 v[74:75], v[14:15], v[80:81]
	v_pk_mul_f32 v[80:81], v[12:13], v[72:73]
	v_pk_add_f32 v[72:73], v[114:115], 1.0 op_sel_hi:[1,0]
	v_pk_add_f32 v[82:83], v[112:113], 1.0 op_sel_hi:[1,0]
	v_pk_fma_f32 v[72:73], v[72:73], v[74:75], v[110:111]
	v_pk_fma_f32 v[74:75], v[82:83], v[80:81], v[108:109]
	s_mov_b64 s[2:3], -1
	v_cvt_pk_bf16_f32 v80, v74, v75
	v_cvt_pk_bf16_f32 v81, v72, v73
	s_cbranch_vccnz .LBB0_434
	s_mov_b64 s[2:3], 0
	global_store_dwordx2 v[76:77], v[80:81], off offset:1536

.LBB0_579:
	s_waitcnt vmcnt(0)
	v_add_u32_e32 v12, s13, v88
	v_add_u32_e32 v4, 0x45, v12
	v_ashrrev_i32_e32 v13, 31, v12
	v_ashrrev_i32_e32 v5, 31, v4
	v_lshlrev_b64 v[0:1], 13, v[12:13]
	v_lshlrev_b64 v[4:5], 13, v[4:5]
	v_lshl_add_u64 v[0:1], v[64:65], 0, v[0:1]
	v_lshl_add_u64 v[4:5], v[64:65], 0, v[4:5]
	global_load_dwordx4 v[48:51], v[0:1], off nt
	v_add_u32_e32 v8, 0x46, v12
	global_load_dwordx4 v[4:7], v[4:5], off nt
	v_or_b32_e32 v0, 1, v12
	v_ashrrev_i32_e32 v1, 31, v0
	v_ashrrev_i32_e32 v9, 31, v8
	v_lshlrev_b64 v[0:1], 13, v[0:1]
	v_lshlrev_b64 v[8:9], 13, v[8:9]
	v_lshl_add_u64 v[0:1], v[64:65], 0, v[0:1]
	v_lshl_add_u64 v[8:9], v[64:65], 0, v[8:9]
	global_load_dwordx4 v[52:55], v[0:1], off nt
	global_load_dwordx4 v[8:11], v[8:9], off nt
	v_or_b32_e32 v0, 2, v12
	v_ashrrev_i32_e32 v1, 31, v0
	v_lshlrev_b64 v[0:1], 13, v[0:1]
	v_lshl_add_u64 v[0:1], v[64:65], 0, v[0:1]
	global_load_dwordx4 v[56:59], v[0:1], off nt
	v_or_b32_e32 v0, 3, v12
	v_ashrrev_i32_e32 v1, 31, v0
	v_lshlrev_b64 v[0:1], 13, v[0:1]
	v_lshl_add_u64 v[0:1], v[64:65], 0, v[0:1]
	global_load_dwordx4 v[60:63], v[0:1], off nt
	v_or_b32_e32 v0, 4, v12
	v_ashrrev_i32_e32 v1, 31, v0
	v_lshlrev_b64 v[0:1], 13, v[0:1]
	v_lshl_add_u64 v[0:1], v[64:65], 0, v[0:1]
	global_load_dwordx4 v[32:35], v[0:1], off nt
	v_or_b32_e32 v0, 5, v12
	v_ashrrev_i32_e32 v1, 31, v0
	v_lshlrev_b64 v[0:1], 13, v[0:1]
	v_lshl_add_u64 v[0:1], v[64:65], 0, v[0:1]
	global_load_dwordx4 v[36:39], v[0:1], off nt
	v_or_b32_e32 v0, 6, v12
	v_ashrrev_i32_e32 v1, 31, v0
	v_lshlrev_b64 v[0:1], 13, v[0:1]
	v_lshl_add_u64 v[0:1], v[64:65], 0, v[0:1]
	global_load_dwordx4 v[40:43], v[0:1], off nt
	v_or_b32_e32 v0, 7, v12
	v_ashrrev_i32_e32 v1, 31, v0
	v_lshlrev_b64 v[0:1], 13, v[0:1]
	v_lshl_add_u64 v[0:1], v[64:65], 0, v[0:1]
	global_load_dwordx4 v[44:47], v[0:1], off nt
	v_add_u32_e32 v0, 64, v12
	v_ashrrev_i32_e32 v1, 31, v0
	v_lshlrev_b64 v[0:1], 13, v[0:1]
	v_lshl_add_u64 v[0:1], v[64:65], 0, v[0:1]
	global_load_dwordx4 v[16:19], v[0:1], off nt
	v_add_u32_e32 v0, 0x41, v12
	v_ashrrev_i32_e32 v1, 31, v0
	v_lshlrev_b64 v[0:1], 13, v[0:1]
	v_lshl_add_u64 v[0:1], v[64:65], 0, v[0:1]
	global_load_dwordx4 v[20:23], v[0:1], off nt
	v_add_u32_e32 v0, 0x42, v12
	v_ashrrev_i32_e32 v1, 31, v0
	v_lshlrev_b64 v[0:1], 13, v[0:1]
	v_lshl_add_u64 v[0:1], v[64:65], 0, v[0:1]
	global_load_dwordx4 v[24:27], v[0:1], off nt
	v_add_u32_e32 v0, 0x43, v12
	v_ashrrev_i32_e32 v1, 31, v0
	v_lshlrev_b64 v[0:1], 13, v[0:1]
	v_lshl_add_u64 v[0:1], v[64:65], 0, v[0:1]
	global_load_dwordx4 v[28:31], v[0:1], off nt
	v_add_u32_e32 v0, 0x44, v12
	v_ashrrev_i32_e32 v1, 31, v0
	v_lshlrev_b64 v[0:1], 13, v[0:1]
	v_lshl_add_u64 v[0:1], v[64:65], 0, v[0:1]
	global_load_dwordx4 v[0:3], v[0:1], off nt
	v_add_u32_e32 v12, 0x47, v12
	v_ashrrev_i32_e32 v13, 31, v12
	v_lshlrev_b64 v[12:13], 13, v[12:13]
	v_lshl_add_u64 v[12:13], v[64:65], 0, v[12:13]
	global_load_dwordx4 v[12:15], v[12:13], off nt
	s_and_b64 vcc, exec, s[10:11]
	s_mov_b64 s[10:11], 0
	s_waitcnt vmcnt(15)
	v_mul_f32_e32 v48, 0x42000000, v48
	s_waitcnt vmcnt(14)
	v_mul_f32_e32 v4, 0x42000000, v4
	v_mul_f32_e32 v5, 0x42000000, v5
	s_waitcnt vmcnt(13)
	v_mul_f32_e32 v52, 0x42000000, v52
	v_cvt_pk_fp8_f32 v66, v48, v52
	s_waitcnt vmcnt(12)
	v_mul_f32_e32 v8, 0x42000000, v8
	s_waitcnt vmcnt(11)
	v_mul_f32_e32 v48, 0x42000000, v57
	v_mul_f32_e32 v56, 0x42000000, v56
	s_waitcnt vmcnt(10)
	v_mul_f32_e32 v60, 0x42000000, v60
	v_cvt_pk_fp8_f32 v66, v56, v60 op_sel:[0,0,1]
	s_waitcnt vmcnt(9)
	v_mul_f32_e32 v32, 0x42000000, v32
	s_waitcnt vmcnt(8)
	v_mul_f32_e32 v36, 0x42000000, v36
	v_cvt_pk_fp8_f32 v67, v32, v36
	v_mul_f32_e32 v32, 0x42000000, v49
	v_mul_f32_e32 v36, 0x42000000, v53
	v_mul_f32_e32 v49, 0x42000000, v61
	s_waitcnt vmcnt(7)
	v_mul_f32_e32 v40, 0x42000000, v40
	s_waitcnt vmcnt(6)
	v_mul_f32_e32 v44, 0x42000000, v44
	v_cvt_pk_fp8_f32 v67, v40, v44 op_sel:[0,0,1]
	v_cvt_pk_fp8_f32 v40, v32, v36
	v_mul_f32_e32 v32, 0x42000000, v33
	v_mul_f32_e32 v33, 0x42000000, v37
	v_mul_f32_e32 v36, 0x42000000, v41
	v_cvt_pk_fp8_f32 v41, v32, v33
	v_mul_f32_e32 v37, 0x42000000, v45
	v_mul_f32_e32 v32, 0x42000000, v50
	v_mul_f32_e32 v33, 0x42000000, v54
	v_cvt_pk_fp8_f32 v41, v36, v37 op_sel:[0,0,1]
	v_cvt_pk_fp8_f32 v36, v32, v33
	v_mul_f32_e32 v37, 0x42000000, v58
	v_mul_f32_e32 v45, 0x42000000, v62
	v_mul_f32_e32 v32, 0x42000000, v34
	v_cvt_pk_fp8_f32 v36, v37, v45 op_sel:[0,0,1]
	v_mul_f32_e32 v33, 0x42000000, v38
	v_cvt_pk_fp8_f32 v37, v32, v33
	v_mul_f32_e32 v34, 0x42000000, v42
	v_mul_f32_e32 v38, 0x42000000, v46
	v_mul_f32_e32 v33, 0x42000000, v51
	v_cvt_pk_fp8_f32 v37, v34, v38 op_sel:[0,0,1]
	v_mul_f32_e32 v34, 0x42000000, v55
	v_cvt_pk_fp8_f32 v32, v33, v34
	v_mul_f32_e32 v34, 0x42000000, v35
	v_mul_f32_e32 v35, 0x42000000, v39
	v_cvt_pk_fp8_f32 v33, v34, v35
	s_waitcnt vmcnt(1)
	v_mul_f32_e32 v0, 0x42000000, v0
	v_cvt_pk_fp8_f32 v35, v0, v4
	s_waitcnt vmcnt(0)
	v_mul_f32_e32 v12, 0x42000000, v12
	v_mul_f32_e32 v4, 0x42000000, v17
	v_cvt_pk_fp8_f32 v35, v8, v12 op_sel:[0,0,1]
	v_mul_f32_e32 v8, 0x42000000, v21
	v_cvt_pk_fp8_f32 v0, v4, v8
	v_mul_f32_e32 v4, 0x42000000, v1
	v_cvt_pk_fp8_f32 v1, v4, v5
	v_mul_f32_e32 v16, 0x42000000, v16
	v_mul_f32_e32 v20, 0x42000000, v20
	v_cvt_pk_fp8_f32 v34, v16, v20
	v_mul_f32_e32 v12, 0x42000000, v25
	v_mul_f32_e32 v16, 0x42000000, v29
	v_mul_f32_e32 v8, 0x42000000, v9
	v_mul_f32_e32 v9, 0x42000000, v13
	v_cvt_pk_fp8_f32 v40, v48, v49 op_sel:[0,0,1]
	v_cvt_pk_fp8_f32 v0, v12, v16 op_sel:[0,0,1]
	v_cvt_pk_fp8_f32 v1, v8, v9 op_sel:[0,0,1]
	v_add_u32_e32 v44, s13, v76
	v_mul_f32_e32 v4, 0x42000000, v22
	v_mul_f32_e32 v2, 0x42000000, v2
	ds_write2_b64 v44, v[40:41], v[0:1] offset0:34 offset1:42
	v_mul_f32_e32 v1, 0x42000000, v18
	v_cvt_pk_fp8_f32 v0, v1, v4
	v_mul_f32_e32 v4, 0x42000000, v6
	v_cvt_pk_fp8_f32 v1, v2, v4
	v_mul_f32_e32 v5, 0x42000000, v26
	v_mul_f32_e32 v8, 0x42000000, v30
	v_cvt_pk_fp8_f32 v0, v5, v8 op_sel:[0,0,1]
	v_mul_f32_e32 v5, 0x42000000, v10
	v_mul_f32_e32 v6, 0x42000000, v14
	v_cvt_pk_fp8_f32 v1, v5, v6 op_sel:[0,0,1]
	v_mul_f32_e32 v2, 0x42000000, v23
	v_mul_f32_e32 v38, 0x42000000, v59
	v_mul_f32_e32 v42, 0x42000000, v63
	ds_write2_b64 v44, v[36:37], v[0:1] offset0:68 offset1:76
	v_mul_f32_e32 v1, 0x42000000, v19
	v_cvt_pk_fp8_f32 v0, v1, v2
	v_mul_f32_e32 v2, 0x42000000, v3
	v_mul_f32_e32 v3, 0x42000000, v7
	v_cvt_pk_fp8_f32 v1, v2, v3
	v_mul_f32_e32 v4, 0x42000000, v27
	v_mul_f32_e32 v5, 0x42000000, v31
	v_cvt_pk_fp8_f32 v32, v38, v42 op_sel:[0,0,1]
	v_mul_f32_e32 v38, 0x42000000, v43
	v_mul_f32_e32 v39, 0x42000000, v47
	v_mul_f32_e32 v24, 0x42000000, v24
	v_mul_f32_e32 v28, 0x42000000, v28
	v_cvt_pk_fp8_f32 v0, v4, v5 op_sel:[0,0,1]
	v_mul_f32_e32 v4, 0x42000000, v11
	v_mul_f32_e32 v5, 0x42000000, v15
	v_cvt_pk_fp8_f32 v33, v38, v39 op_sel:[0,0,1]
	v_cvt_pk_fp8_f32 v34, v24, v28 op_sel:[0,0,1]
	v_cvt_pk_fp8_f32 v1, v4, v5 op_sel:[0,0,1]
	s_movk_i32 s13, 0x80
	ds_write2_b64 v44, v[66:67], v[34:35] offset1:8
	ds_write2_b64 v44, v[32:33], v[0:1] offset0:102 offset1:110
	s_cbranch_vccnz .LBB0_579
	s_lshl_b64 s[8:9], s[8:9], 21
	s_add_u32 s8, s95, s8
	s_addc_u32 s9, s97, s9
	s_lshl_b32 s2, s2, 8
	s_waitcnt lgkmcnt(0)
	s_barrier
	v_add_u32_e32 v88, v80, v172
	s_ashr_i32 s10, s3, 31
	ds_read_b128 v[0:3], v88
	v_add_u32_e32 v4, s2, v75
	s_add_u32 s8, s8, s3
	v_ashrrev_i32_e32 v5, 31, v4
	s_addc_u32 s9, s9, s10
	v_lshlrev_b64 v[4:5], 10, v[4:5]
	v_lshl_add_u64 v[4:5], s[8:9], 0, v[4:5]
	v_lshl_add_u64 v[4:5], v[4:5], 0, v[172:173]
	v_add_u32_e32 v89, v81, v172
	s_waitcnt lgkmcnt(0)
	global_store_dwordx4 v[4:5], v[0:3], off sc1
	ds_read_b128 v[0:3], v89
	v_add_u32_e32 v4, s2, v74
	v_ashrrev_i32_e32 v5, 31, v4
	v_lshlrev_b64 v[4:5], 10, v[4:5]
	v_lshl_add_u64 v[4:5], s[8:9], 0, v[4:5]
	v_lshl_add_u64 v[4:5], v[4:5], 0, v[172:173]
	v_add_u32_e32 v90, v82, v172
	s_waitcnt lgkmcnt(0)
	global_store_dwordx4 v[4:5], v[0:3], off sc1
	ds_read_b128 v[0:3], v90
	v_add_u32_e32 v4, s2, v73
	v_ashrrev_i32_e32 v5, 31, v4
	v_lshlrev_b64 v[4:5], 10, v[4:5]
	v_lshl_add_u64 v[4:5], s[8:9], 0, v[4:5]
	v_lshl_add_u64 v[4:5], v[4:5], 0, v[172:173]
	v_add_u32_e32 v91, v83, v172
	s_waitcnt lgkmcnt(0)
	global_store_dwordx4 v[4:5], v[0:3], off sc1
	ds_read_b128 v[0:3], v91
	v_add_u32_e32 v4, s2, v72
	v_ashrrev_i32_e32 v5, 31, v4
	v_lshlrev_b64 v[4:5], 10, v[4:5]
	v_lshl_add_u64 v[4:5], s[8:9], 0, v[4:5]
	v_lshl_add_u64 v[4:5], v[4:5], 0, v[172:173]
	v_add_u32_e32 v92, v84, v172
	s_waitcnt lgkmcnt(0)
	global_store_dwordx4 v[4:5], v[0:3], off sc1
	ds_read_b128 v[0:3], v92
	v_add_u32_e32 v4, s2, v71
	v_ashrrev_i32_e32 v5, 31, v4
	v_lshlrev_b64 v[4:5], 10, v[4:5]
	v_lshl_add_u64 v[4:5], s[8:9], 0, v[4:5]
	v_lshl_add_u64 v[4:5], v[4:5], 0, v[172:173]
	v_add_u32_e32 v93, v85, v172
	s_waitcnt lgkmcnt(0)
	global_store_dwordx4 v[4:5], v[0:3], off sc1
	ds_read_b128 v[0:3], v93
	v_add_u32_e32 v4, s2, v70
	v_ashrrev_i32_e32 v5, 31, v4
	v_lshlrev_b64 v[4:5], 10, v[4:5]
	v_lshl_add_u64 v[4:5], s[8:9], 0, v[4:5]
	v_lshl_add_u64 v[4:5], v[4:5], 0, v[172:173]
	v_add_u32_e32 v94, v86, v172
	s_waitcnt lgkmcnt(0)
	global_store_dwordx4 v[4:5], v[0:3], off sc1
	ds_read_b128 v[0:3], v94
	v_add_u32_e32 v4, s2, v69
	v_ashrrev_i32_e32 v5, 31, v4
	v_lshlrev_b64 v[4:5], 10, v[4:5]
	v_lshl_add_u64 v[4:5], s[8:9], 0, v[4:5]
	v_lshl_add_u64 v[4:5], v[4:5], 0, v[172:173]
	v_add_u32_e32 v95, v87, v172
	s_waitcnt lgkmcnt(0)
	global_store_dwordx4 v[4:5], v[0:3], off sc1
	ds_read_b128 v[0:3], v95
	v_add_u32_e32 v4, s2, v68
	v_ashrrev_i32_e32 v5, 31, v4
	v_lshlrev_b64 v[4:5], 10, v[4:5]
	v_lshl_add_u64 v[4:5], s[8:9], 0, v[4:5]
	v_lshl_add_u64 v[4:5], v[4:5], 0, v[172:173]
	s_waitcnt lgkmcnt(0)
	global_store_dwordx4 v[4:5], v[0:3], off sc1
	s_waitcnt lgkmcnt(0)
	s_barrier
	s_movk_i32 s8, 0xff60
	s_mov_b64 s[2:3], 0
	s_and_b64 vcc, exec, s[6:7]
	s_cbranch_vccz .LBB0_578
	v_readlane_b32 s0, v250, 60
	s_add_i32 s2, s0, s1
	s_ashr_i32 s3, s2, 31
	v_readlane_b32 s8, v255, 19
	s_lshl_b64 s[4:5], s[2:3], 20
	s_lshl_b64 s[2:3], s[2:3], 22
	v_readlane_b32 s14, v255, 25
	v_readlane_b32 s0, v250, 61
	v_readlane_b32 s15, v255, 26
	s_add_u32 s2, s14, s2
	v_or_b32_e32 v0, s0, v77
	s_addc_u32 s3, s15, s3
	v_readlane_b32 s0, v250, 63
	v_ashrrev_i32_e32 v1, 31, v0
	v_lshl_add_u64 v[64:65], v[0:1], 2, s[2:3]
	v_add_u32_e32 v77, s0, v78
	s_mov_b32 s1, 0
	s_mov_b64 s[6:7], -1
	v_readlane_b32 s9, v255, 20
	v_readlane_b32 s10, v255, 21
	v_readlane_b32 s11, v255, 22
	v_readlane_b32 s12, v255, 23
	v_readlane_b32 s13, v255, 24
.LBB0_582:
	v_add_u32_e32 v12, s1, v77
	v_add_u32_e32 v4, 0x45, v12
	v_ashrrev_i32_e32 v13, 31, v12
	v_ashrrev_i32_e32 v5, 31, v4
	v_lshlrev_b64 v[0:1], 12, v[12:13]
	v_lshlrev_b64 v[4:5], 12, v[4:5]
	v_lshl_add_u64 v[0:1], v[64:65], 0, v[0:1]
	v_lshl_add_u64 v[4:5], v[64:65], 0, v[4:5]
	global_load_dwordx4 v[48:51], v[0:1], off nt
	v_add_u32_e32 v8, 0x46, v12
	global_load_dwordx4 v[4:7], v[4:5], off nt
	v_or_b32_e32 v0, 1, v12
	v_ashrrev_i32_e32 v1, 31, v0
	v_ashrrev_i32_e32 v9, 31, v8
	v_lshlrev_b64 v[0:1], 12, v[0:1]
	v_lshlrev_b64 v[8:9], 12, v[8:9]
	v_lshl_add_u64 v[0:1], v[64:65], 0, v[0:1]
	v_lshl_add_u64 v[8:9], v[64:65], 0, v[8:9]
	global_load_dwordx4 v[52:55], v[0:1], off nt
	global_load_dwordx4 v[8:11], v[8:9], off nt
	v_or_b32_e32 v0, 2, v12
	v_ashrrev_i32_e32 v1, 31, v0
	v_lshlrev_b64 v[0:1], 12, v[0:1]
	v_lshl_add_u64 v[0:1], v[64:65], 0, v[0:1]
	global_load_dwordx4 v[56:59], v[0:1], off nt
	v_or_b32_e32 v0, 3, v12
	v_ashrrev_i32_e32 v1, 31, v0
	v_lshlrev_b64 v[0:1], 12, v[0:1]
	v_lshl_add_u64 v[0:1], v[64:65], 0, v[0:1]
	global_load_dwordx4 v[60:63], v[0:1], off nt
	v_or_b32_e32 v0, 4, v12
	v_ashrrev_i32_e32 v1, 31, v0
	v_lshlrev_b64 v[0:1], 12, v[0:1]
	v_lshl_add_u64 v[0:1], v[64:65], 0, v[0:1]
	global_load_dwordx4 v[32:35], v[0:1], off nt
	v_or_b32_e32 v0, 5, v12
	v_ashrrev_i32_e32 v1, 31, v0
	v_lshlrev_b64 v[0:1], 12, v[0:1]
	v_lshl_add_u64 v[0:1], v[64:65], 0, v[0:1]
	global_load_dwordx4 v[36:39], v[0:1], off nt
	v_or_b32_e32 v0, 6, v12
	v_ashrrev_i32_e32 v1, 31, v0
	v_lshlrev_b64 v[0:1], 12, v[0:1]
	v_lshl_add_u64 v[0:1], v[64:65], 0, v[0:1]
	global_load_dwordx4 v[40:43], v[0:1], off nt
	v_or_b32_e32 v0, 7, v12
	v_ashrrev_i32_e32 v1, 31, v0
	v_lshlrev_b64 v[0:1], 12, v[0:1]
	v_lshl_add_u64 v[0:1], v[64:65], 0, v[0:1]
	global_load_dwordx4 v[44:47], v[0:1], off nt
	v_add_u32_e32 v0, 64, v12
	v_ashrrev_i32_e32 v1, 31, v0
	v_lshlrev_b64 v[0:1], 12, v[0:1]
	v_lshl_add_u64 v[0:1], v[64:65], 0, v[0:1]
	global_load_dwordx4 v[16:19], v[0:1], off nt
	v_add_u32_e32 v0, 0x41, v12
	v_ashrrev_i32_e32 v1, 31, v0
	v_lshlrev_b64 v[0:1], 12, v[0:1]
	v_lshl_add_u64 v[0:1], v[64:65], 0, v[0:1]
	global_load_dwordx4 v[20:23], v[0:1], off nt
	v_add_u32_e32 v0, 0x42, v12
	v_ashrrev_i32_e32 v1, 31, v0
	v_lshlrev_b64 v[0:1], 12, v[0:1]
	v_lshl_add_u64 v[0:1], v[64:65], 0, v[0:1]
	global_load_dwordx4 v[24:27], v[0:1], off nt
	v_add_u32_e32 v0, 0x43, v12
	v_ashrrev_i32_e32 v1, 31, v0
	v_lshlrev_b64 v[0:1], 12, v[0:1]
	v_lshl_add_u64 v[0:1], v[64:65], 0, v[0:1]
	global_load_dwordx4 v[28:31], v[0:1], off nt
	v_add_u32_e32 v0, 0x44, v12
	v_ashrrev_i32_e32 v1, 31, v0
	v_lshlrev_b64 v[0:1], 12, v[0:1]
	v_lshl_add_u64 v[0:1], v[64:65], 0, v[0:1]
	global_load_dwordx4 v[0:3], v[0:1], off nt
	v_add_u32_e32 v12, 0x47, v12
	v_ashrrev_i32_e32 v13, 31, v12
	v_lshlrev_b64 v[12:13], 12, v[12:13]
	v_lshl_add_u64 v[12:13], v[64:65], 0, v[12:13]
	global_load_dwordx4 v[12:15], v[12:13], off nt
	s_and_b64 vcc, exec, s[6:7]
	s_mov_b64 s[6:7], 0
	s_waitcnt vmcnt(15)
	v_mul_f32_e32 v48, 0x42000000, v48
	s_waitcnt vmcnt(14)
	v_mul_f32_e32 v4, 0x42000000, v4
	v_mul_f32_e32 v5, 0x42000000, v5
	s_waitcnt vmcnt(13)
	v_mul_f32_e32 v52, 0x42000000, v52
	v_cvt_pk_fp8_f32 v66, v48, v52
	s_waitcnt vmcnt(12)
	v_mul_f32_e32 v8, 0x42000000, v8
	s_waitcnt vmcnt(11)
	v_mul_f32_e32 v48, 0x42000000, v57
	v_mul_f32_e32 v56, 0x42000000, v56
	s_waitcnt vmcnt(10)
	v_mul_f32_e32 v60, 0x42000000, v60
	v_cvt_pk_fp8_f32 v66, v56, v60 op_sel:[0,0,1]
	s_waitcnt vmcnt(9)
	v_mul_f32_e32 v32, 0x42000000, v32
	s_waitcnt vmcnt(8)
	v_mul_f32_e32 v36, 0x42000000, v36
	v_cvt_pk_fp8_f32 v67, v32, v36
	v_mul_f32_e32 v32, 0x42000000, v49
	v_mul_f32_e32 v36, 0x42000000, v53
	v_mul_f32_e32 v49, 0x42000000, v61
	s_waitcnt vmcnt(7)
	v_mul_f32_e32 v40, 0x42000000, v40
	s_waitcnt vmcnt(6)
	v_mul_f32_e32 v44, 0x42000000, v44
	v_cvt_pk_fp8_f32 v67, v40, v44 op_sel:[0,0,1]
	v_cvt_pk_fp8_f32 v40, v32, v36
	v_mul_f32_e32 v32, 0x42000000, v33
	v_mul_f32_e32 v33, 0x42000000, v37
	v_mul_f32_e32 v36, 0x42000000, v41
	v_cvt_pk_fp8_f32 v41, v32, v33
	v_mul_f32_e32 v37, 0x42000000, v45
	v_mul_f32_e32 v32, 0x42000000, v50
	v_mul_f32_e32 v33, 0x42000000, v54
	v_cvt_pk_fp8_f32 v41, v36, v37 op_sel:[0,0,1]
	v_cvt_pk_fp8_f32 v36, v32, v33
	v_mul_f32_e32 v37, 0x42000000, v58
	v_mul_f32_e32 v45, 0x42000000, v62
	v_mul_f32_e32 v32, 0x42000000, v34
	v_cvt_pk_fp8_f32 v36, v37, v45 op_sel:[0,0,1]
	v_mul_f32_e32 v33, 0x42000000, v38
	v_cvt_pk_fp8_f32 v37, v32, v33
	v_mul_f32_e32 v34, 0x42000000, v42
	v_mul_f32_e32 v38, 0x42000000, v46
	v_mul_f32_e32 v33, 0x42000000, v51
	v_cvt_pk_fp8_f32 v37, v34, v38 op_sel:[0,0,1]
	v_mul_f32_e32 v34, 0x42000000, v55
	v_cvt_pk_fp8_f32 v32, v33, v34
	v_mul_f32_e32 v34, 0x42000000, v35
	v_mul_f32_e32 v35, 0x42000000, v39
	v_cvt_pk_fp8_f32 v33, v34, v35
	s_waitcnt vmcnt(1)
	v_mul_f32_e32 v0, 0x42000000, v0
	v_cvt_pk_fp8_f32 v35, v0, v4
	s_waitcnt vmcnt(0)
	v_mul_f32_e32 v12, 0x42000000, v12
	v_mul_f32_e32 v4, 0x42000000, v17
	v_cvt_pk_fp8_f32 v35, v8, v12 op_sel:[0,0,1]
	v_mul_f32_e32 v8, 0x42000000, v21
	v_cvt_pk_fp8_f32 v0, v4, v8
	v_mul_f32_e32 v4, 0x42000000, v1
	v_cvt_pk_fp8_f32 v1, v4, v5
	v_mul_f32_e32 v16, 0x42000000, v16
	v_mul_f32_e32 v20, 0x42000000, v20
	v_cvt_pk_fp8_f32 v34, v16, v20
	v_mul_f32_e32 v12, 0x42000000, v25
	v_mul_f32_e32 v16, 0x42000000, v29
	v_mul_f32_e32 v8, 0x42000000, v9
	v_mul_f32_e32 v9, 0x42000000, v13
	v_cvt_pk_fp8_f32 v40, v48, v49 op_sel:[0,0,1]
	v_cvt_pk_fp8_f32 v0, v12, v16 op_sel:[0,0,1]
	v_cvt_pk_fp8_f32 v1, v8, v9 op_sel:[0,0,1]
	v_add_u32_e32 v44, s1, v76
	v_mul_f32_e32 v4, 0x42000000, v22
	v_mul_f32_e32 v2, 0x42000000, v2
	ds_write2_b64 v44, v[40:41], v[0:1] offset0:34 offset1:42
	v_mul_f32_e32 v1, 0x42000000, v18
	v_cvt_pk_fp8_f32 v0, v1, v4
	v_mul_f32_e32 v4, 0x42000000, v6
	v_cvt_pk_fp8_f32 v1, v2, v4
	v_mul_f32_e32 v5, 0x42000000, v26
	v_mul_f32_e32 v8, 0x42000000, v30
	v_cvt_pk_fp8_f32 v0, v5, v8 op_sel:[0,0,1]
	v_mul_f32_e32 v5, 0x42000000, v10
	v_mul_f32_e32 v6, 0x42000000, v14
	v_cvt_pk_fp8_f32 v1, v5, v6 op_sel:[0,0,1]
	v_mul_f32_e32 v2, 0x42000000, v23
	v_mul_f32_e32 v38, 0x42000000, v59
	v_mul_f32_e32 v42, 0x42000000, v63
	ds_write2_b64 v44, v[36:37], v[0:1] offset0:68 offset1:76
	v_mul_f32_e32 v1, 0x42000000, v19
	v_cvt_pk_fp8_f32 v0, v1, v2
	v_mul_f32_e32 v2, 0x42000000, v3
	v_mul_f32_e32 v3, 0x42000000, v7
	v_cvt_pk_fp8_f32 v1, v2, v3
	v_mul_f32_e32 v4, 0x42000000, v27
	v_mul_f32_e32 v5, 0x42000000, v31
	v_cvt_pk_fp8_f32 v32, v38, v42 op_sel:[0,0,1]
	v_mul_f32_e32 v38, 0x42000000, v43
	v_mul_f32_e32 v39, 0x42000000, v47
	v_mul_f32_e32 v24, 0x42000000, v24
	v_mul_f32_e32 v28, 0x42000000, v28
	v_cvt_pk_fp8_f32 v0, v4, v5 op_sel:[0,0,1]
	v_mul_f32_e32 v4, 0x42000000, v11
	v_mul_f32_e32 v5, 0x42000000, v15
	v_cvt_pk_fp8_f32 v33, v38, v39 op_sel:[0,0,1]
	v_cvt_pk_fp8_f32 v34, v24, v28 op_sel:[0,0,1]
	v_cvt_pk_fp8_f32 v1, v4, v5 op_sel:[0,0,1]
	s_movk_i32 s1, 0x80
	ds_write2_b64 v44, v[66:67], v[34:35] offset1:8
	ds_write2_b64 v44, v[32:33], v[0:1] offset0:102 offset1:110
	s_cbranch_vccnz .LBB0_582
	v_readlane_b32 s0, v251, 0
	s_add_u32 s2, s0, s4
	v_readlane_b32 s0, v251, 2
	s_waitcnt lgkmcnt(0)
	s_barrier
	s_addc_u32 s3, s0, s5
	v_readlane_b32 s0, v250, 61
	ds_read_b128 v[0:3], v88
	s_nop 0
	v_add_u32_e32 v4, s0, v75
	v_ashrrev_i32_e32 v5, 31, v4
	v_lshlrev_b64 v[4:5], 10, v[4:5]
	v_lshl_add_u64 v[4:5], s[2:3], 0, v[4:5]
	v_lshl_add_u64 v[4:5], v[4:5], 0, v[172:173]
	s_waitcnt lgkmcnt(0)
	global_store_dwordx4 v[4:5], v[0:3], off sc1
	ds_read_b128 v[0:3], v89
	v_add_u32_e32 v4, s0, v74
	v_ashrrev_i32_e32 v5, 31, v4
	v_lshlrev_b64 v[4:5], 10, v[4:5]
	v_lshl_add_u64 v[4:5], s[2:3], 0, v[4:5]
	v_lshl_add_u64 v[4:5], v[4:5], 0, v[172:173]
	s_waitcnt lgkmcnt(0)
	global_store_dwordx4 v[4:5], v[0:3], off sc1
	ds_read_b128 v[0:3], v90
	v_add_u32_e32 v4, s0, v73
	v_ashrrev_i32_e32 v5, 31, v4
	v_lshlrev_b64 v[4:5], 10, v[4:5]
	v_lshl_add_u64 v[4:5], s[2:3], 0, v[4:5]
	v_lshl_add_u64 v[4:5], v[4:5], 0, v[172:173]
	s_waitcnt lgkmcnt(0)
	global_store_dwordx4 v[4:5], v[0:3], off sc1
	ds_read_b128 v[0:3], v91
	v_add_u32_e32 v4, s0, v72
	v_ashrrev_i32_e32 v5, 31, v4
	v_lshlrev_b64 v[4:5], 10, v[4:5]
	v_lshl_add_u64 v[4:5], s[2:3], 0, v[4:5]
	v_lshl_add_u64 v[4:5], v[4:5], 0, v[172:173]
	s_waitcnt lgkmcnt(0)
	global_store_dwordx4 v[4:5], v[0:3], off sc1
	ds_read_b128 v[0:3], v92
	v_add_u32_e32 v4, s0, v71
	v_ashrrev_i32_e32 v5, 31, v4
	v_lshlrev_b64 v[4:5], 10, v[4:5]
	v_lshl_add_u64 v[4:5], s[2:3], 0, v[4:5]
	v_lshl_add_u64 v[4:5], v[4:5], 0, v[172:173]
	s_waitcnt lgkmcnt(0)
	global_store_dwordx4 v[4:5], v[0:3], off sc1
	ds_read_b128 v[0:3], v93
	v_add_u32_e32 v4, s0, v70
	v_ashrrev_i32_e32 v5, 31, v4
	v_lshlrev_b64 v[4:5], 10, v[4:5]
	v_lshl_add_u64 v[4:5], s[2:3], 0, v[4:5]
	v_lshl_add_u64 v[4:5], v[4:5], 0, v[172:173]
	s_waitcnt lgkmcnt(0)
	global_store_dwordx4 v[4:5], v[0:3], off sc1
	ds_read_b128 v[0:3], v94
	v_add_u32_e32 v4, s0, v69
	v_ashrrev_i32_e32 v5, 31, v4
	v_lshlrev_b64 v[4:5], 10, v[4:5]
	v_lshl_add_u64 v[4:5], s[2:3], 0, v[4:5]
	v_lshl_add_u64 v[4:5], v[4:5], 0, v[172:173]
	s_waitcnt lgkmcnt(0)
	global_store_dwordx4 v[4:5], v[0:3], off sc1
	ds_read_b128 v[0:3], v95
	v_add_u32_e32 v4, s0, v68
	v_ashrrev_i32_e32 v5, 31, v4
	v_lshlrev_b64 v[4:5], 10, v[4:5]
	v_lshl_add_u64 v[4:5], s[2:3], 0, v[4:5]
	v_lshl_add_u64 v[4:5], v[4:5], 0, v[172:173]
	s_waitcnt lgkmcnt(0)
	global_store_dwordx4 v[4:5], v[0:3], off sc1
	s_waitcnt lgkmcnt(0)
	s_barrier

.LBB0_1328:
	v_add_u32_e32 v12, s12, v88
	v_add_u32_e32 v4, 0x45, v12
	v_ashrrev_i32_e32 v13, 31, v12
	v_ashrrev_i32_e32 v5, 31, v4
	v_lshlrev_b64 v[0:1], 13, v[12:13]
	v_lshlrev_b64 v[4:5], 13, v[4:5]
	v_lshl_add_u64 v[0:1], v[64:65], 0, v[0:1]
	v_lshl_add_u64 v[4:5], v[64:65], 0, v[4:5]
	global_load_dwordx4 v[48:51], v[0:1], off nt
	v_add_u32_e32 v8, 0x46, v12
	global_load_dwordx4 v[4:7], v[4:5], off nt
	v_or_b32_e32 v0, 1, v12
	v_ashrrev_i32_e32 v1, 31, v0
	v_ashrrev_i32_e32 v9, 31, v8
	v_lshlrev_b64 v[0:1], 13, v[0:1]
	v_lshlrev_b64 v[8:9], 13, v[8:9]
	v_lshl_add_u64 v[0:1], v[64:65], 0, v[0:1]
	v_lshl_add_u64 v[8:9], v[64:65], 0, v[8:9]
	global_load_dwordx4 v[52:55], v[0:1], off nt
	global_load_dwordx4 v[8:11], v[8:9], off nt
	v_or_b32_e32 v0, 2, v12
	v_ashrrev_i32_e32 v1, 31, v0
	v_lshlrev_b64 v[0:1], 13, v[0:1]
	v_lshl_add_u64 v[0:1], v[64:65], 0, v[0:1]
	global_load_dwordx4 v[56:59], v[0:1], off nt
	v_or_b32_e32 v0, 3, v12
	v_ashrrev_i32_e32 v1, 31, v0
	v_lshlrev_b64 v[0:1], 13, v[0:1]
	v_lshl_add_u64 v[0:1], v[64:65], 0, v[0:1]
	global_load_dwordx4 v[60:63], v[0:1], off nt
	v_or_b32_e32 v0, 4, v12
	v_ashrrev_i32_e32 v1, 31, v0
	v_lshlrev_b64 v[0:1], 13, v[0:1]
	v_lshl_add_u64 v[0:1], v[64:65], 0, v[0:1]
	global_load_dwordx4 v[32:35], v[0:1], off nt
	v_or_b32_e32 v0, 5, v12
	v_ashrrev_i32_e32 v1, 31, v0
	v_lshlrev_b64 v[0:1], 13, v[0:1]
	v_lshl_add_u64 v[0:1], v[64:65], 0, v[0:1]
	global_load_dwordx4 v[36:39], v[0:1], off nt
	v_or_b32_e32 v0, 6, v12
	v_ashrrev_i32_e32 v1, 31, v0
	v_lshlrev_b64 v[0:1], 13, v[0:1]
	v_lshl_add_u64 v[0:1], v[64:65], 0, v[0:1]
	global_load_dwordx4 v[40:43], v[0:1], off nt
	v_or_b32_e32 v0, 7, v12
	v_ashrrev_i32_e32 v1, 31, v0
	v_lshlrev_b64 v[0:1], 13, v[0:1]
	v_lshl_add_u64 v[0:1], v[64:65], 0, v[0:1]
	global_load_dwordx4 v[44:47], v[0:1], off nt
	v_add_u32_e32 v0, 64, v12
	v_ashrrev_i32_e32 v1, 31, v0
	v_lshlrev_b64 v[0:1], 13, v[0:1]
	v_lshl_add_u64 v[0:1], v[64:65], 0, v[0:1]
	global_load_dwordx4 v[16:19], v[0:1], off nt
	v_add_u32_e32 v0, 0x41, v12
	v_ashrrev_i32_e32 v1, 31, v0
	v_lshlrev_b64 v[0:1], 13, v[0:1]
	v_lshl_add_u64 v[0:1], v[64:65], 0, v[0:1]
	global_load_dwordx4 v[20:23], v[0:1], off nt
	v_add_u32_e32 v0, 0x42, v12
	v_ashrrev_i32_e32 v1, 31, v0
	v_lshlrev_b64 v[0:1], 13, v[0:1]
	v_lshl_add_u64 v[0:1], v[64:65], 0, v[0:1]
	global_load_dwordx4 v[24:27], v[0:1], off nt
	v_add_u32_e32 v0, 0x43, v12
	v_ashrrev_i32_e32 v1, 31, v0
	v_lshlrev_b64 v[0:1], 13, v[0:1]
	v_lshl_add_u64 v[0:1], v[64:65], 0, v[0:1]
	global_load_dwordx4 v[28:31], v[0:1], off nt
	v_add_u32_e32 v0, 0x44, v12
	v_ashrrev_i32_e32 v1, 31, v0
	v_lshlrev_b64 v[0:1], 13, v[0:1]
	v_lshl_add_u64 v[0:1], v[64:65], 0, v[0:1]
	global_load_dwordx4 v[0:3], v[0:1], off nt
	v_add_u32_e32 v12, 0x47, v12
	v_ashrrev_i32_e32 v13, 31, v12
	v_lshlrev_b64 v[12:13], 13, v[12:13]
	v_lshl_add_u64 v[12:13], v[64:65], 0, v[12:13]
	global_load_dwordx4 v[12:15], v[12:13], off nt
	s_and_b64 vcc, exec, s[10:11]
	s_mov_b64 s[10:11], 0
	s_waitcnt vmcnt(15)
	v_mul_f32_e32 v48, 0x42000000, v48
	s_waitcnt vmcnt(14)
	v_mul_f32_e32 v4, 0x42000000, v4
	v_mul_f32_e32 v5, 0x42000000, v5
	s_waitcnt vmcnt(13)
	v_mul_f32_e32 v52, 0x42000000, v52
	v_cvt_pk_fp8_f32 v66, v48, v52
	s_waitcnt vmcnt(12)
	v_mul_f32_e32 v8, 0x42000000, v8
	s_waitcnt vmcnt(11)
	v_mul_f32_e32 v48, 0x42000000, v57
	v_mul_f32_e32 v56, 0x42000000, v56
	s_waitcnt vmcnt(10)
	v_mul_f32_e32 v60, 0x42000000, v60
	v_cvt_pk_fp8_f32 v66, v56, v60 op_sel:[0,0,1]
	s_waitcnt vmcnt(9)
	v_mul_f32_e32 v32, 0x42000000, v32
	s_waitcnt vmcnt(8)
	v_mul_f32_e32 v36, 0x42000000, v36
	v_cvt_pk_fp8_f32 v67, v32, v36
	v_mul_f32_e32 v32, 0x42000000, v49
	v_mul_f32_e32 v36, 0x42000000, v53
	v_mul_f32_e32 v49, 0x42000000, v61
	s_waitcnt vmcnt(7)
	v_mul_f32_e32 v40, 0x42000000, v40
	s_waitcnt vmcnt(6)
	v_mul_f32_e32 v44, 0x42000000, v44
	v_cvt_pk_fp8_f32 v67, v40, v44 op_sel:[0,0,1]
	v_cvt_pk_fp8_f32 v40, v32, v36
	v_mul_f32_e32 v32, 0x42000000, v33
	v_mul_f32_e32 v33, 0x42000000, v37
	v_mul_f32_e32 v36, 0x42000000, v41
	v_cvt_pk_fp8_f32 v41, v32, v33
	v_mul_f32_e32 v37, 0x42000000, v45
	v_mul_f32_e32 v32, 0x42000000, v50
	v_mul_f32_e32 v33, 0x42000000, v54
	v_cvt_pk_fp8_f32 v41, v36, v37 op_sel:[0,0,1]
	v_cvt_pk_fp8_f32 v36, v32, v33
	v_mul_f32_e32 v37, 0x42000000, v58
	v_mul_f32_e32 v45, 0x42000000, v62
	v_mul_f32_e32 v32, 0x42000000, v34
	v_cvt_pk_fp8_f32 v36, v37, v45 op_sel:[0,0,1]
	v_mul_f32_e32 v33, 0x42000000, v38
	v_cvt_pk_fp8_f32 v37, v32, v33
	v_mul_f32_e32 v34, 0x42000000, v42
	v_mul_f32_e32 v38, 0x42000000, v46
	v_mul_f32_e32 v33, 0x42000000, v51
	v_cvt_pk_fp8_f32 v37, v34, v38 op_sel:[0,0,1]
	v_mul_f32_e32 v34, 0x42000000, v55
	v_cvt_pk_fp8_f32 v32, v33, v34
	v_mul_f32_e32 v34, 0x42000000, v35
	v_mul_f32_e32 v35, 0x42000000, v39
	v_cvt_pk_fp8_f32 v33, v34, v35
	s_waitcnt vmcnt(1)
	v_mul_f32_e32 v0, 0x42000000, v0
	v_cvt_pk_fp8_f32 v35, v0, v4
	s_waitcnt vmcnt(0)
	v_mul_f32_e32 v12, 0x42000000, v12
	v_mul_f32_e32 v4, 0x42000000, v17
	v_cvt_pk_fp8_f32 v35, v8, v12 op_sel:[0,0,1]
	v_mul_f32_e32 v8, 0x42000000, v21
	v_cvt_pk_fp8_f32 v0, v4, v8
	v_mul_f32_e32 v4, 0x42000000, v1
	v_cvt_pk_fp8_f32 v1, v4, v5
	v_mul_f32_e32 v16, 0x42000000, v16
	v_mul_f32_e32 v20, 0x42000000, v20
	v_cvt_pk_fp8_f32 v34, v16, v20
	v_mul_f32_e32 v12, 0x42000000, v25
	v_mul_f32_e32 v16, 0x42000000, v29
	v_mul_f32_e32 v8, 0x42000000, v9
	v_mul_f32_e32 v9, 0x42000000, v13
	v_cvt_pk_fp8_f32 v40, v48, v49 op_sel:[0,0,1]
	v_cvt_pk_fp8_f32 v0, v12, v16 op_sel:[0,0,1]
	v_cvt_pk_fp8_f32 v1, v8, v9 op_sel:[0,0,1]
	v_add_u32_e32 v44, s12, v79
	v_mul_f32_e32 v4, 0x42000000, v22
	v_mul_f32_e32 v2, 0x42000000, v2
	ds_write2_b64 v44, v[40:41], v[0:1] offset0:34 offset1:42
	v_mul_f32_e32 v1, 0x42000000, v18
	v_cvt_pk_fp8_f32 v0, v1, v4
	v_mul_f32_e32 v4, 0x42000000, v6
	v_cvt_pk_fp8_f32 v1, v2, v4
	v_mul_f32_e32 v5, 0x42000000, v26
	v_mul_f32_e32 v8, 0x42000000, v30
	v_cvt_pk_fp8_f32 v0, v5, v8 op_sel:[0,0,1]
	v_mul_f32_e32 v5, 0x42000000, v10
	v_mul_f32_e32 v6, 0x42000000, v14
	v_cvt_pk_fp8_f32 v1, v5, v6 op_sel:[0,0,1]
	v_mul_f32_e32 v2, 0x42000000, v23
	v_mul_f32_e32 v38, 0x42000000, v59
	v_mul_f32_e32 v42, 0x42000000, v63
	ds_write2_b64 v44, v[36:37], v[0:1] offset0:68 offset1:76
	v_mul_f32_e32 v1, 0x42000000, v19
	v_cvt_pk_fp8_f32 v0, v1, v2
	v_mul_f32_e32 v2, 0x42000000, v3
	v_mul_f32_e32 v3, 0x42000000, v7
	v_cvt_pk_fp8_f32 v1, v2, v3
	v_mul_f32_e32 v4, 0x42000000, v27
	v_mul_f32_e32 v5, 0x42000000, v31
	v_cvt_pk_fp8_f32 v32, v38, v42 op_sel:[0,0,1]
	v_mul_f32_e32 v38, 0x42000000, v43
	v_mul_f32_e32 v39, 0x42000000, v47
	v_mul_f32_e32 v24, 0x42000000, v24
	v_mul_f32_e32 v28, 0x42000000, v28
	v_cvt_pk_fp8_f32 v0, v4, v5 op_sel:[0,0,1]
	v_mul_f32_e32 v4, 0x42000000, v11
	v_mul_f32_e32 v5, 0x42000000, v15
	v_cvt_pk_fp8_f32 v33, v38, v39 op_sel:[0,0,1]
	v_cvt_pk_fp8_f32 v34, v24, v28 op_sel:[0,0,1]
	v_cvt_pk_fp8_f32 v1, v4, v5 op_sel:[0,0,1]
	s_movk_i32 s12, 0x80
	ds_write2_b64 v44, v[66:67], v[34:35] offset1:8
	ds_write2_b64 v44, v[32:33], v[0:1] offset0:102 offset1:110
	s_cbranch_vccnz .LBB0_1328
	s_lshl_b64 s[8:9], s[8:9], 21
	s_add_u32 s8, s95, s8
	s_addc_u32 s9, s97, s9
	s_lshl_b32 s10, s2, 8
	s_waitcnt lgkmcnt(0)
	s_barrier
	s_ashr_i32 s11, s3, 31
	ds_read_b128 v[0:3], v80
	v_add_u32_e32 v4, s10, v71
	s_add_u32 s2, s8, s3
	v_ashrrev_i32_e32 v5, 31, v4
	s_addc_u32 s3, s9, s11
	v_lshlrev_b64 v[4:5], 10, v[4:5]
	v_lshl_add_u64 v[4:5], s[2:3], 0, v[4:5]
	v_lshl_add_u64 v[4:5], v[4:5], 0, v[172:173]
	s_waitcnt lgkmcnt(0)
	global_store_dwordx4 v[4:5], v[0:3], off sc1
	ds_read_b128 v[0:3], v81
	v_add_u32_e32 v4, s10, v72
	v_ashrrev_i32_e32 v5, 31, v4
	v_lshlrev_b64 v[4:5], 10, v[4:5]
	v_lshl_add_u64 v[4:5], s[2:3], 0, v[4:5]
	v_lshl_add_u64 v[4:5], v[4:5], 0, v[172:173]
	s_waitcnt lgkmcnt(0)
	global_store_dwordx4 v[4:5], v[0:3], off sc1
	ds_read_b128 v[0:3], v82
	v_add_u32_e32 v4, s10, v73
	v_ashrrev_i32_e32 v5, 31, v4
	v_lshlrev_b64 v[4:5], 10, v[4:5]
	v_lshl_add_u64 v[4:5], s[2:3], 0, v[4:5]
	v_lshl_add_u64 v[4:5], v[4:5], 0, v[172:173]
	s_waitcnt lgkmcnt(0)
	global_store_dwordx4 v[4:5], v[0:3], off sc1
	ds_read_b128 v[0:3], v83
	v_add_u32_e32 v4, s10, v74
	v_ashrrev_i32_e32 v5, 31, v4
	v_lshlrev_b64 v[4:5], 10, v[4:5]
	v_lshl_add_u64 v[4:5], s[2:3], 0, v[4:5]
	v_lshl_add_u64 v[4:5], v[4:5], 0, v[172:173]
	s_waitcnt lgkmcnt(0)
	global_store_dwordx4 v[4:5], v[0:3], off sc1
	ds_read_b128 v[0:3], v84
	v_add_u32_e32 v4, s10, v75
	v_ashrrev_i32_e32 v5, 31, v4
	v_lshlrev_b64 v[4:5], 10, v[4:5]
	v_lshl_add_u64 v[4:5], s[2:3], 0, v[4:5]
	v_lshl_add_u64 v[4:5], v[4:5], 0, v[172:173]
	s_waitcnt lgkmcnt(0)
	global_store_dwordx4 v[4:5], v[0:3], off sc1
	ds_read_b128 v[0:3], v85
	v_add_u32_e32 v4, s10, v76
	v_ashrrev_i32_e32 v5, 31, v4
	v_lshlrev_b64 v[4:5], 10, v[4:5]
	v_lshl_add_u64 v[4:5], s[2:3], 0, v[4:5]
	v_lshl_add_u64 v[4:5], v[4:5], 0, v[172:173]
	s_waitcnt lgkmcnt(0)
	global_store_dwordx4 v[4:5], v[0:3], off sc1
	ds_read_b128 v[0:3], v86
	v_add_u32_e32 v4, s10, v77
	v_ashrrev_i32_e32 v5, 31, v4
	v_lshlrev_b64 v[4:5], 10, v[4:5]
	v_lshl_add_u64 v[4:5], s[2:3], 0, v[4:5]
	v_lshl_add_u64 v[4:5], v[4:5], 0, v[172:173]
	s_waitcnt lgkmcnt(0)
	global_store_dwordx4 v[4:5], v[0:3], off sc1
	ds_read_b128 v[0:3], v87
	v_add_u32_e32 v4, s10, v78
	v_ashrrev_i32_e32 v5, 31, v4
	v_lshlrev_b64 v[4:5], 10, v[4:5]
	v_lshl_add_u64 v[4:5], s[2:3], 0, v[4:5]
	v_lshl_add_u64 v[4:5], v[4:5], 0, v[172:173]
	s_waitcnt lgkmcnt(0)
	global_store_dwordx4 v[4:5], v[0:3], off sc1
	s_waitcnt lgkmcnt(0)
	s_barrier
	s_movk_i32 s8, 0xc0
	s_mov_b64 s[2:3], 0
	s_andn2_b64 vcc, exec, s[6:7]
	s_cbranch_vccnz .LBB0_1327

.LBB0_1396:
	v_fma_f32 v156, s22, v212, v198
	s_mov_b32 s0, 0x800000
	v_cmp_gt_f32_e32 vcc, s0, v156
	v_mul_f32_e32 v158, 0x4b800000, v156
	s_waitcnt vmcnt(0)
	v_pk_add_f32 v[114:115], v[114:115], 1.0 op_sel_hi:[1,0]
	v_cndmask_b32_e32 v156, v156, v158, vcc
	v_rsq_f32_e32 v156, v156
	v_pk_add_f32 v[186:187], v[112:113], 1.0 op_sel_hi:[1,0]
	s_cmp_lt_i32 s21, s1
	s_cselect_b64 s[10:11], -1, 0
	v_mul_f32_e32 v158, 0x45800000, v156
	v_cndmask_b32_e32 v174, v156, v158, vcc
	v_pk_mul_f32 v[178:179], v[174:175], v[178:179] op_sel_hi:[0,1]
	v_pk_mul_f32 v[176:177], v[174:175], v[176:177] op_sel_hi:[0,1]
	v_pk_mul_f32 v[176:177], v[0:1], v[176:177]
	v_pk_mul_f32 v[178:179], v[2:3], v[178:179]
	s_ashr_i32 s7, s6, 31
	v_pk_fma_f32 v[112:113], v[178:179], v[114:115], v[118:119]
	v_pk_fma_f32 v[114:115], v[176:177], v[186:187], v[116:117]
	v_cvt_pk_fp8_f32 v116, v114, v115
	s_lshl_b64 s[2:3], s[6:7], 10
	v_readlane_b32 s6, v253, 44
	v_readlane_b32 s7, v253, 45
	v_cvt_pk_fp8_f32 v116, v112, v113 op_sel:[0,0,1]
	s_add_u32 s6, s6, s2
	s_addc_u32 s7, s7, s3
	s_cmp_ge_i32 s21, s1
	v_lshl_add_u64 v[176:177], s[6:7], 0, v[122:123]
	s_cbranch_scc1 .LBB0_1398
	global_store_dword v[176:177], v116, off

.LBB0_1402:
	v_mov_b32_e32 v175, v174
	v_mov_b32_e32 v178, v169
	v_mov_b32_e32 v169, v170
	v_pk_mul_f32 v[168:169], v[174:175], v[168:169]
	s_waitcnt vmcnt(0)
	v_pk_add_f32 v[112:113], v[112:113], 1.0 op_sel_hi:[1,0]
	v_pk_mul_f32 v[168:169], v[4:5], v[168:169]
	v_mov_b32_e32 v179, v171
	v_pk_fma_f32 v[112:113], v[168:169], v[112:113], v[116:117]
	v_mov_b32_e32 v186, v174
	v_mov_b32_e32 v187, v174
	v_cvt_pk_fp8_f32 v116, v112, v113
	v_pk_mul_f32 v[178:179], v[186:187], v[178:179]
	v_pk_add_f32 v[114:115], v[114:115], 1.0 op_sel_hi:[1,0]
	v_pk_mul_f32 v[168:169], v[6:7], v[178:179]
	v_cndmask_b32_e64 v117, 0, 1, s[10:11]
	v_pk_fma_f32 v[114:115], v[168:169], v[114:115], v[118:119]
	v_cmp_ne_u32_e64 s[6:7], 1, v117
	v_cvt_pk_fp8_f32 v116, v114, v115 op_sel:[0,0,1]
	s_andn2_b64 vcc, exec, s[10:11]
	s_cbranch_vccnz .LBB0_1404
	global_store_dword v[176:177], v116, off offset:256

.LBB0_1408:
	v_pk_mul_f32 v[162:163], v[174:175], v[162:163]
	s_waitcnt vmcnt(0)
	v_pk_add_f32 v[112:113], v[112:113], 1.0 op_sel_hi:[1,0]
	v_pk_mul_f32 v[162:163], v[8:9], v[162:163]
	v_mov_b32_e32 v168, v174
	v_pk_fma_f32 v[112:113], v[162:163], v[112:113], v[116:117]
	v_mov_b32_e32 v169, v174
	v_cvt_pk_fp8_f32 v116, v112, v113
	v_pk_mul_f32 v[164:165], v[168:169], v[164:165]
	v_pk_add_f32 v[114:115], v[114:115], 1.0 op_sel_hi:[1,0]
	v_pk_mul_f32 v[162:163], v[10:11], v[164:165]
	s_and_b64 vcc, exec, s[6:7]
	v_pk_fma_f32 v[114:115], v[162:163], v[114:115], v[118:119]
	s_nop 0
	v_cvt_pk_fp8_f32 v116, v114, v115 op_sel:[0,0,1]
	s_cbranch_vccnz .LBB0_1410
	global_store_dword v[176:177], v116, off offset:512

.LBB0_1414:
	v_mov_b32_e32 v156, v159
	v_pk_mul_f32 v[156:157], v[156:157], v[174:175]
	s_waitcnt vmcnt(0)
	v_pk_add_f32 v[112:113], v[112:113], 1.0 op_sel_hi:[1,0]
	v_pk_mul_f32 v[156:157], v[12:13], v[156:157]
	v_mov_b32_e32 v162, v174
	v_pk_fma_f32 v[112:113], v[156:157], v[112:113], v[116:117]
	v_mov_b32_e32 v163, v174
	v_cvt_pk_fp8_f32 v116, v112, v113
	v_pk_mul_f32 v[160:161], v[160:161], v[162:163]
	v_pk_add_f32 v[114:115], v[114:115], 1.0 op_sel_hi:[1,0]
	v_pk_mul_f32 v[156:157], v[14:15], v[160:161]
	s_and_b64 vcc, exec, s[6:7]
	v_pk_fma_f32 v[114:115], v[156:157], v[114:115], v[118:119]
	s_nop 0
	v_cvt_pk_fp8_f32 v116, v114, v115 op_sel:[0,0,1]
	s_cbranch_vccnz .LBB0_1416
	global_store_dword v[176:177], v116, off offset:768

.LBB0_1420:
	v_fma_f32 v156, s22, v212, v198
	v_cmp_gt_f32_e32 vcc, s0, v156
	v_mul_f32_e32 v158, 0x4b800000, v156
	s_waitcnt vmcnt(0)
	v_pk_add_f32 v[114:115], v[114:115], 1.0 op_sel_hi:[1,0]
	v_cndmask_b32_e32 v156, v156, v158, vcc
	v_rsq_f32_e32 v156, v156
	v_pk_add_f32 v[170:171], v[112:113], 1.0 op_sel_hi:[1,0]
	s_cmp_lt_i32 s21, s1
	s_cselect_b64 s[10:11], -1, 0
	v_mul_f32_e32 v158, 0x45800000, v156
	v_cndmask_b32_e32 v164, v156, v158, vcc
	v_pk_mul_f32 v[168:169], v[164:165], v[168:169] op_sel_hi:[0,1]
	v_pk_mul_f32 v[166:167], v[164:165], v[166:167] op_sel_hi:[0,1]
	v_pk_mul_f32 v[166:167], v[0:1], v[166:167]
	v_pk_mul_f32 v[168:169], v[2:3], v[168:169]
	s_ashr_i32 s7, s6, 31
	v_pk_fma_f32 v[112:113], v[168:169], v[114:115], v[118:119]
	v_pk_fma_f32 v[114:115], v[166:167], v[170:171], v[116:117]
	v_cvt_pk_fp8_f32 v116, v114, v115
	s_lshl_b64 s[2:3], s[6:7], 10
	v_readlane_b32 s6, v253, 44
	v_readlane_b32 s7, v253, 45
	v_cvt_pk_fp8_f32 v116, v112, v113 op_sel:[0,0,1]
	s_add_u32 s6, s6, s2
	s_addc_u32 s7, s7, s3
	s_cmp_ge_i32 s21, s1
	v_lshl_add_u64 v[166:167], s[6:7], 0, v[122:123]
	s_cbranch_scc1 .LBB0_1422
	global_store_dword v[166:167], v116, off

.LBB0_1426:
	v_mov_b32_e32 v165, v164
	v_mov_b32_e32 v168, v161
	v_mov_b32_e32 v161, v162
	v_pk_mul_f32 v[160:161], v[164:165], v[160:161]
	s_waitcnt vmcnt(0)
	v_pk_add_f32 v[112:113], v[112:113], 1.0 op_sel_hi:[1,0]
	v_pk_mul_f32 v[160:161], v[4:5], v[160:161]
	v_mov_b32_e32 v169, v163
	v_pk_fma_f32 v[112:113], v[160:161], v[112:113], v[116:117]
	v_mov_b32_e32 v170, v164
	v_mov_b32_e32 v171, v164
	v_cvt_pk_fp8_f32 v116, v112, v113
	v_pk_mul_f32 v[168:169], v[170:171], v[168:169]
	v_pk_add_f32 v[114:115], v[114:115], 1.0 op_sel_hi:[1,0]
	v_pk_mul_f32 v[160:161], v[6:7], v[168:169]
	v_cndmask_b32_e64 v117, 0, 1, s[10:11]
	v_pk_fma_f32 v[114:115], v[160:161], v[114:115], v[118:119]
	v_cmp_ne_u32_e64 s[6:7], 1, v117
	v_cvt_pk_fp8_f32 v116, v114, v115 op_sel:[0,0,1]
	s_andn2_b64 vcc, exec, s[10:11]
	s_cbranch_vccnz .LBB0_1428
	global_store_dword v[166:167], v116, off offset:256

.LBB0_1432:
	v_pk_mul_f32 v[150:151], v[164:165], v[150:151]
	s_waitcnt vmcnt(0)
	v_pk_add_f32 v[112:113], v[112:113], 1.0 op_sel_hi:[1,0]
	v_pk_mul_f32 v[150:151], v[8:9], v[150:151]
	v_mov_b32_e32 v160, v164
	v_pk_fma_f32 v[112:113], v[150:151], v[112:113], v[116:117]
	v_mov_b32_e32 v161, v164
	v_cvt_pk_fp8_f32 v116, v112, v113
	v_pk_mul_f32 v[148:149], v[160:161], v[148:149]
	v_pk_add_f32 v[114:115], v[114:115], 1.0 op_sel_hi:[1,0]
	v_pk_mul_f32 v[148:149], v[10:11], v[148:149]
	s_and_b64 vcc, exec, s[6:7]
	v_pk_fma_f32 v[114:115], v[148:149], v[114:115], v[118:119]
	s_nop 0
	v_cvt_pk_fp8_f32 v116, v114, v115 op_sel:[0,0,1]
	s_cbranch_vccnz .LBB0_1434
	global_store_dword v[166:167], v116, off offset:512

.LBB0_1438:
	v_mov_b32_e32 v156, v159
	v_pk_mul_f32 v[150:151], v[156:157], v[164:165]
	s_waitcnt vmcnt(0)
	v_pk_add_f32 v[112:113], v[112:113], 1.0 op_sel_hi:[1,0]
	v_pk_mul_f32 v[150:151], v[12:13], v[150:151]
	v_mov_b32_e32 v148, v164
	v_pk_fma_f32 v[112:113], v[150:151], v[112:113], v[116:117]
	v_mov_b32_e32 v149, v164
	v_cvt_pk_fp8_f32 v116, v112, v113
	v_pk_mul_f32 v[148:149], v[154:155], v[148:149]
	v_pk_add_f32 v[114:115], v[114:115], 1.0 op_sel_hi:[1,0]
	v_pk_mul_f32 v[148:149], v[14:15], v[148:149]
	s_and_b64 vcc, exec, s[6:7]
	v_pk_fma_f32 v[114:115], v[148:149], v[114:115], v[118:119]
	s_nop 0
	v_cvt_pk_fp8_f32 v116, v114, v115 op_sel:[0,0,1]
	s_cbranch_vccnz .LBB0_1391
	global_store_dword v[166:167], v116, off offset:768
	s_branch .LBB0_1391

.LBB0_1540:
	s_mul_hi_u32 s2, s57, 0xaaaaaaab
	s_lshr_b32 s2, s2, 1
	s_mul_i32 s2, s2, 3
	s_sub_i32 s2, s57, s2
	s_nop 15
	s_nop 15
	v_lshl_add_u32 v6, s2, 10, v195
	ds_read_b128 v[12:15], v6
	ds_read_b128 v[0:3], v6 offset:16
	ds_read_b128 v[8:11], v6 offset:512
	v_readlane_b32 s2, v253, 54
	s_waitcnt lgkmcnt(0)
	v_pk_fma_f32 v[4:5], v[156:157], s[38:39], v[12:13] op_sel_hi:[1,0,1]
	v_pk_fma_f32 v[22:23], v[152:153], s[38:39], v[8:9] op_sel_hi:[1,0,1]
	v_min_f32_e32 v17, 0x40e00000, v5
	v_min_f32_e32 v16, 0x40e00000, v4
	v_pk_mul_f32 v[4:5], v[16:17], s[88:89] op_sel_hi:[1,0]
	v_med3_f32 v23, v23, s55, v213
	v_exp_f32_e32 v20, v4
	v_exp_f32_e32 v21, v5
	v_med3_f32 v22, v22, s55, v213
	v_pk_add_f32 v[22:23], v[22:23], 1.0 op_sel_hi:[1,0]
	v_pk_fma_f32 v[24:25], v[154:155], s[38:39], v[10:11] op_sel_hi:[1,0,1]
	v_pk_add_f32 v[20:21], v[20:21], 1.0 op_sel_hi:[1,0]
	v_pk_mul_f32 v[16:17], v[16:17], v[22:23]
	v_rcp_f32_e32 v20, v20
	v_rcp_f32_e32 v21, v21
	v_med3_f32 v25, v25, s55, v213
	v_med3_f32 v24, v24, s55, v213
	v_pk_add_f32 v[24:25], v[24:25], 1.0 op_sel_hi:[1,0]
	v_pk_mul_f32 v[16:17], v[16:17], v[20:21]
	v_pk_fma_f32 v[20:21], v[158:159], s[38:39], v[14:15] op_sel_hi:[1,0,1]
	ds_read_b128 v[4:7], v6 offset:528
	v_min_f32_e32 v21, 0x40e00000, v21
	v_min_f32_e32 v20, 0x40e00000, v20
	v_pk_mul_f32 v[22:23], v[20:21], s[88:89] op_sel_hi:[1,0]
	v_pk_mul_f32 v[20:21], v[20:21], v[24:25]
	v_exp_f32_e32 v22, v22
	v_exp_f32_e32 v23, v23
	v_pk_fma_f32 v[24:25], v[148:149], s[38:39], v[0:1] op_sel_hi:[1,0,1]
	s_waitcnt lgkmcnt(0)
	v_pk_fma_f32 v[28:29], v[146:147], s[38:39], v[6:7] op_sel_hi:[1,0,1]
	v_min_f32_e32 v25, 0x40e00000, v25
	v_min_f32_e32 v24, 0x40e00000, v24
	v_pk_add_f32 v[22:23], v[22:23], 1.0 op_sel_hi:[1,0]
	v_pk_mul_f32 v[26:27], v[24:25], s[88:89] op_sel_hi:[1,0]
	v_rcp_f32_e32 v22, v22
	v_rcp_f32_e32 v23, v23
	v_exp_f32_e32 v26, v26
	v_exp_f32_e32 v27, v27
	v_med3_f32 v29, v29, s55, v213
	v_pk_mul_f32 v[20:21], v[20:21], v[22:23]
	v_pk_fma_f32 v[22:23], v[144:145], s[38:39], v[4:5] op_sel_hi:[1,0,1]
	v_pk_add_f32 v[26:27], v[26:27], 1.0 op_sel_hi:[1,0]
	v_med3_f32 v23, v23, s55, v213
	v_rcp_f32_e32 v26, v26
	v_rcp_f32_e32 v27, v27
	v_med3_f32 v22, v22, s55, v213
	v_pk_add_f32 v[22:23], v[22:23], 1.0 op_sel_hi:[1,0]
	v_med3_f32 v28, v28, s55, v213
	v_pk_mul_f32 v[22:23], v[24:25], v[22:23]
	v_pk_fma_f32 v[24:25], v[150:151], s[38:39], v[2:3] op_sel_hi:[1,0,1]
	v_pk_mul_f32 v[22:23], v[22:23], v[26:27]
	v_min_f32_e32 v25, 0x40e00000, v25
	v_min_f32_e32 v24, 0x40e00000, v24
	v_pk_mul_f32 v[26:27], v[24:25], s[88:89] op_sel_hi:[1,0]
	v_pk_add_f32 v[28:29], v[28:29], 1.0 op_sel_hi:[1,0]
	v_exp_f32_e32 v26, v26
	v_exp_f32_e32 v27, v27
	v_cvt_pk_fp8_f32 v30, v16, v17
	v_pk_mul_f32 v[16:17], v[24:25], v[28:29]
	v_pk_fma_f32 v[24:25], v[140:141], s[38:39], v[12:13] op_sel_hi:[1,0,1]
	v_pk_add_f32 v[26:27], v[26:27], 1.0 op_sel_hi:[1,0]
	v_min_f32_e32 v25, 0x40e00000, v25
	v_rcp_f32_e32 v26, v26
	v_rcp_f32_e32 v27, v27
	v_min_f32_e32 v24, 0x40e00000, v24
	v_cvt_pk_fp8_f32 v31, v22, v23
	v_pk_fma_f32 v[28:29], v[136:137], s[38:39], v[8:9] op_sel_hi:[1,0,1]
	v_pk_mul_f32 v[16:17], v[16:17], v[26:27]
	v_pk_mul_f32 v[26:27], v[24:25], s[88:89] op_sel_hi:[1,0]
	v_med3_f32 v29, v29, s55, v213
	v_exp_f32_e32 v26, v26
	v_exp_f32_e32 v27, v27
	v_med3_f32 v28, v28, s55, v213
	v_cvt_pk_fp8_f32 v30, v20, v21 op_sel:[0,0,1]
	v_cvt_pk_fp8_f32 v31, v16, v17 op_sel:[0,0,1]
	v_pk_add_f32 v[26:27], v[26:27], 1.0 op_sel_hi:[1,0]
	v_pk_add_f32 v[28:29], v[28:29], 1.0 op_sel_hi:[1,0]
	v_rcp_f32_e32 v26, v26
	v_rcp_f32_e32 v27, v27
	v_pk_mul_f32 v[24:25], v[24:25], v[28:29]
	ds_bpermute_b32 v22, v167, v30
	ds_bpermute_b32 v23, v167, v31
	v_pk_mul_f32 v[24:25], v[24:25], v[26:27]
	v_pk_fma_f32 v[26:27], v[142:143], s[38:39], v[14:15] op_sel_hi:[1,0,1]
	v_pk_fma_f32 v[30:31], v[138:139], s[38:39], v[10:11] op_sel_hi:[1,0,1]
	v_min_f32_e32 v27, 0x40e00000, v27
	v_min_f32_e32 v26, 0x40e00000, v26
	v_pk_mul_f32 v[28:29], v[26:27], s[88:89] op_sel_hi:[1,0]
	v_med3_f32 v31, v31, s55, v213
	v_exp_f32_e32 v28, v28
	v_exp_f32_e32 v29, v29
	v_med3_f32 v30, v30, s55, v213
	v_pk_add_f32 v[30:31], v[30:31], 1.0 op_sel_hi:[1,0]
	v_lshl_add_u32 v20, v219, 8, v171
	v_pk_mul_f32 v[26:27], v[26:27], v[30:31]
	v_pk_fma_f32 v[30:31], v[132:133], s[38:39], v[0:1] op_sel_hi:[1,0,1]
	v_pk_add_f32 v[28:29], v[28:29], 1.0 op_sel_hi:[1,0]
	v_min_f32_e32 v31, 0x40e00000, v31
	v_min_f32_e32 v30, 0x40e00000, v30
	v_pk_mul_f32 v[132:133], v[30:31], s[88:89] op_sel_hi:[1,0]
	v_rcp_f32_e32 v28, v28
	v_rcp_f32_e32 v29, v29
	v_exp_f32_e32 v132, v132
	v_exp_f32_e32 v133, v133
	v_ashrrev_i32_e32 v21, 31, v20
	v_lshlrev_b64 v[16:17], 10, v[20:21]
	v_pk_mul_f32 v[26:27], v[26:27], v[28:29]
	v_pk_fma_f32 v[28:29], v[128:129], s[38:39], v[4:5] op_sel_hi:[1,0,1]
	v_pk_add_f32 v[128:129], v[132:133], 1.0 op_sel_hi:[1,0]
	v_cvt_pk_fp8_f32 v21, v24, v25
	v_rcp_f32_e32 v128, v128
	v_rcp_f32_e32 v129, v129
	v_med3_f32 v29, v29, s55, v213
	v_med3_f32 v28, v28, s55, v213
	v_pk_add_f32 v[28:29], v[28:29], 1.0 op_sel_hi:[1,0]
	v_cvt_pk_fp8_f32 v21, v26, v27 op_sel:[0,0,1]
	v_pk_mul_f32 v[28:29], v[30:31], v[28:29]
	v_pk_fma_f32 v[26:27], v[124:125], s[38:39], v[12:13] op_sel_hi:[1,0,1]
	v_pk_mul_f32 v[28:29], v[28:29], v[128:129]
	v_mov_b32_e32 v132, v173
	v_min_f32_e32 v27, 0x40e00000, v27
	v_min_f32_e32 v26, 0x40e00000, v26
	v_cvt_pk_fp8_f32 v132, v28, v29
	v_pk_mul_f32 v[28:29], v[26:27], s[88:89] op_sel_hi:[1,0]
	v_pk_fma_f32 v[130:131], v[130:131], s[38:39], v[6:7] op_sel_hi:[1,0,1]
	v_exp_f32_e32 v28, v28
	v_exp_f32_e32 v29, v29
	v_pk_fma_f32 v[30:31], v[134:135], s[38:39], v[2:3] op_sel_hi:[1,0,1]
	v_med3_f32 v131, v131, s55, v213
	v_med3_f32 v130, v130, s55, v213
	v_min_f32_e32 v31, 0x40e00000, v31
	v_min_f32_e32 v30, 0x40e00000, v30
	v_pk_add_f32 v[130:131], v[130:131], 1.0 op_sel_hi:[1,0]
	v_pk_add_f32 v[28:29], v[28:29], 1.0 op_sel_hi:[1,0]
	v_pk_mul_f32 v[128:129], v[30:31], s[88:89] op_sel_hi:[1,0]
	v_pk_mul_f32 v[24:25], v[30:31], v[130:131]
	v_pk_fma_f32 v[30:31], v[120:121], s[38:39], v[8:9] op_sel_hi:[1,0,1]
	v_rcp_f32_e32 v28, v28
	v_rcp_f32_e32 v29, v29
	v_med3_f32 v31, v31, s55, v213
	v_med3_f32 v30, v30, s55, v213
	v_pk_add_f32 v[30:31], v[30:31], 1.0 op_sel_hi:[1,0]
	v_pk_fma_f32 v[120:121], v[122:123], s[38:39], v[10:11] op_sel_hi:[1,0,1]
	v_pk_mul_f32 v[26:27], v[26:27], v[30:31]
	v_med3_f32 v121, v121, s55, v213
	v_pk_mul_f32 v[26:27], v[26:27], v[28:29]
	v_pk_fma_f32 v[28:29], v[126:127], s[38:39], v[14:15] op_sel_hi:[1,0,1]
	v_med3_f32 v120, v120, s55, v213
	v_min_f32_e32 v29, 0x40e00000, v29
	v_min_f32_e32 v28, 0x40e00000, v28
	v_pk_mul_f32 v[30:31], v[28:29], s[88:89] op_sel_hi:[1,0]
	v_pk_fma_f32 v[116:117], v[116:117], s[38:39], v[0:1] op_sel_hi:[1,0,1]
	v_exp_f32_e32 v30, v30
	v_exp_f32_e32 v31, v31
	v_pk_add_f32 v[120:121], v[120:121], 1.0 op_sel_hi:[1,0]
	v_min_f32_e32 v117, 0x40e00000, v117
	v_min_f32_e32 v116, 0x40e00000, v116
	v_pk_add_f32 v[30:31], v[30:31], 1.0 op_sel_hi:[1,0]
	v_pk_mul_f32 v[28:29], v[28:29], v[120:121]
	v_pk_mul_f32 v[120:121], v[116:117], s[88:89] op_sel_hi:[1,0]
	v_rcp_f32_e32 v30, v30
	v_rcp_f32_e32 v31, v31
	v_exp_f32_e32 v120, v120
	v_exp_f32_e32 v121, v121
	v_lshl_or_b32 v18, v220, 7, v194
	v_pk_mul_f32 v[28:29], v[28:29], v[30:31]
	v_pk_fma_f32 v[30:31], v[112:113], s[38:39], v[4:5] op_sel_hi:[1,0,1]
	v_pk_add_f32 v[112:113], v[120:121], 1.0 op_sel_hi:[1,0]
	v_med3_f32 v31, v31, s55, v213
	v_rcp_f32_e32 v112, v112
	v_rcp_f32_e32 v113, v113
	v_med3_f32 v30, v30, s55, v213
	v_pk_add_f32 v[30:31], v[30:31], 1.0 op_sel_hi:[1,0]
	v_readlane_b32 s3, v253, 55
	v_pk_mul_f32 v[30:31], v[116:117], v[30:31]
	v_ashrrev_i32_e32 v19, 31, v18
	v_pk_mul_f32 v[30:31], v[30:31], v[112:113]
	v_pk_fma_f32 v[112:113], v[118:119], s[38:39], v[2:3] op_sel_hi:[1,0,1]
	v_lshl_add_u64 v[16:17], s[2:3], 0, v[16:17]
	v_min_f32_e32 v113, 0x40e00000, v113
	v_min_f32_e32 v112, 0x40e00000, v112
	v_pk_mul_f32 v[116:117], v[112:113], s[88:89] op_sel_hi:[1,0]
	v_pk_fma_f32 v[114:115], v[114:115], s[38:39], v[6:7] op_sel_hi:[1,0,1]
	v_exp_f32_e32 v116, v116
	v_exp_f32_e32 v117, v117
	v_lshl_add_u64 v[16:17], v[16:17], 0, v[18:19]
	v_med3_f32 v115, v115, s55, v213
	v_pk_add_f32 v[116:117], v[116:117], 1.0 op_sel_hi:[1,0]
	v_med3_f32 v114, v114, s55, v213
	v_rcp_f32_e32 v116, v116
	v_rcp_f32_e32 v117, v117
	v_cvt_pk_fp8_f32 v118, v30, v31
	s_waitcnt lgkmcnt(0)
	global_store_dwordx2 v[16:17], v[22:23], off
	ds_bpermute_b32 v22, v167, v21
	v_pk_add_f32 v[114:115], v[114:115], 1.0 op_sel_hi:[1,0]
	v_cvt_pk_fp8_f32 v21, v26, v27
	v_pk_mul_f32 v[26:27], v[112:113], v[114:115]
	v_pk_fma_f32 v[30:31], v[104:105], s[38:39], v[8:9] op_sel_hi:[1,0,1]
	v_pk_mul_f32 v[26:27], v[26:27], v[116:117]
	v_cvt_pk_fp8_f32 v21, v28, v29 op_sel:[0,0,1]
	v_cvt_pk_fp8_f32 v118, v26, v27 op_sel:[0,0,1]
	v_pk_fma_f32 v[26:27], v[108:109], s[38:39], v[12:13] op_sel_hi:[1,0,1]
	v_med3_f32 v31, v31, s55, v213
	v_min_f32_e32 v27, 0x40e00000, v27
	v_min_f32_e32 v26, 0x40e00000, v26
	v_pk_mul_f32 v[28:29], v[26:27], s[88:89] op_sel_hi:[1,0]
	v_med3_f32 v30, v30, s55, v213
	v_exp_f32_e32 v28, v28
	v_exp_f32_e32 v29, v29
	v_pk_add_f32 v[30:31], v[30:31], 1.0 op_sel_hi:[1,0]
	v_exp_f32_e32 v128, v128
	v_pk_mul_f32 v[26:27], v[26:27], v[30:31]
	v_pk_add_f32 v[28:29], v[28:29], 1.0 op_sel_hi:[1,0]
	v_exp_f32_e32 v129, v129
	v_rcp_f32_e32 v28, v28
	v_rcp_f32_e32 v29, v29
	v_pk_fma_f32 v[104:105], v[106:107], s[38:39], v[10:11] op_sel_hi:[1,0,1]
	v_pk_add_f32 v[128:129], v[128:129], 1.0 op_sel_hi:[1,0]
	v_med3_f32 v105, v105, s55, v213
	v_pk_mul_f32 v[26:27], v[26:27], v[28:29]
	v_pk_fma_f32 v[28:29], v[110:111], s[38:39], v[14:15] op_sel_hi:[1,0,1]
	v_med3_f32 v104, v104, s55, v213
	v_min_f32_e32 v29, 0x40e00000, v29
	v_min_f32_e32 v28, 0x40e00000, v28
	v_pk_mul_f32 v[30:31], v[28:29], s[88:89] op_sel_hi:[1,0]
	v_pk_fma_f32 v[100:101], v[100:101], s[38:39], v[0:1] op_sel_hi:[1,0,1]
	v_exp_f32_e32 v30, v30
	v_exp_f32_e32 v31, v31
	v_rcp_f32_e32 v128, v128
	v_rcp_f32_e32 v129, v129
	v_pk_add_f32 v[104:105], v[104:105], 1.0 op_sel_hi:[1,0]
	v_min_f32_e32 v101, 0x40e00000, v101
	v_min_f32_e32 v100, 0x40e00000, v100
	v_pk_add_f32 v[30:31], v[30:31], 1.0 op_sel_hi:[1,0]
	v_pk_mul_f32 v[28:29], v[28:29], v[104:105]
	v_pk_mul_f32 v[104:105], v[100:101], s[88:89] op_sel_hi:[1,0]
	v_rcp_f32_e32 v30, v30
	v_rcp_f32_e32 v31, v31
	v_exp_f32_e32 v104, v104
	v_exp_f32_e32 v105, v105
	v_pk_mul_f32 v[24:25], v[24:25], v[128:129]
	v_pk_mul_f32 v[28:29], v[28:29], v[30:31]
	v_cvt_pk_fp8_f32 v132, v24, v25 op_sel:[0,0,1]
	v_pk_fma_f32 v[30:31], v[96:97], s[38:39], v[4:5] op_sel_hi:[1,0,1]
	v_pk_add_f32 v[96:97], v[104:105], 1.0 op_sel_hi:[1,0]
	v_med3_f32 v31, v31, s55, v213
	v_rcp_f32_e32 v96, v96
	v_rcp_f32_e32 v97, v97
	v_med3_f32 v30, v30, s55, v213
	ds_bpermute_b32 v23, v167, v132
	v_or_b32_e32 v24, 16, v20
	v_pk_add_f32 v[30:31], v[30:31], 1.0 op_sel_hi:[1,0]
	v_ashrrev_i32_e32 v25, 31, v24
	v_pk_mul_f32 v[30:31], v[100:101], v[30:31]
	v_lshlrev_b64 v[24:25], 10, v[24:25]
	v_pk_mul_f32 v[30:31], v[30:31], v[96:97]
	v_pk_fma_f32 v[96:97], v[102:103], s[38:39], v[2:3] op_sel_hi:[1,0,1]
	v_lshl_add_u64 v[24:25], s[2:3], 0, v[24:25]
	v_min_f32_e32 v97, 0x40e00000, v97
	v_min_f32_e32 v96, 0x40e00000, v96
	v_lshl_add_u64 v[24:25], v[24:25], 0, v[18:19]
	v_pk_mul_f32 v[100:101], v[96:97], s[88:89] op_sel_hi:[1,0]
	s_waitcnt lgkmcnt(0)
	global_store_dwordx2 v[24:25], v[22:23], off
	ds_bpermute_b32 v22, v167, v21
	v_exp_f32_e32 v100, v100
	v_exp_f32_e32 v101, v101
	v_cvt_pk_fp8_f32 v21, v26, v27
	ds_bpermute_b32 v23, v167, v118
	v_or_b32_e32 v24, 32, v20
	v_pk_add_f32 v[100:101], v[100:101], 1.0 op_sel_hi:[1,0]
	v_ashrrev_i32_e32 v25, 31, v24
	v_pk_fma_f32 v[98:99], v[98:99], s[38:39], v[6:7] op_sel_hi:[1,0,1]
	v_rcp_f32_e32 v100, v100
	v_rcp_f32_e32 v101, v101
	v_cvt_pk_fp8_f32 v21, v28, v29 op_sel:[0,0,1]
	v_lshlrev_b64 v[24:25], 10, v[24:25]
	v_med3_f32 v99, v99, s55, v213
	v_med3_f32 v98, v98, s55, v213
	v_cvt_pk_fp8_f32 v102, v30, v31
	v_lshl_add_u64 v[24:25], s[2:3], 0, v[24:25]
	v_pk_add_f32 v[98:99], v[98:99], 1.0 op_sel_hi:[1,0]
	v_lshl_add_u64 v[24:25], v[24:25], 0, v[18:19]
	v_pk_mul_f32 v[26:27], v[96:97], v[98:99]
	v_or_b32_e32 v20, 48, v20
	v_pk_mul_f32 v[26:27], v[26:27], v[100:101]
	s_waitcnt lgkmcnt(0)
	global_store_dwordx2 v[24:25], v[22:23], off
	ds_bpermute_b32 v22, v167, v21
	v_ashrrev_i32_e32 v21, 31, v20
	v_cvt_pk_fp8_f32 v102, v26, v27 op_sel:[0,0,1]
	v_lshlrev_b64 v[20:21], 10, v[20:21]
	v_lshl_add_u64 v[20:21], s[2:3], 0, v[20:21]
	v_lshl_add_u64 v[18:19], v[20:21], 0, v[18:19]
	v_pk_fma_f32 v[20:21], v[92:93], s[38:39], v[12:13] op_sel_hi:[1,0,1]
	ds_bpermute_b32 v23, v167, v102
	v_min_f32_e32 v21, 0x40e00000, v21
	v_min_f32_e32 v20, 0x40e00000, v20
	v_pk_mul_f32 v[24:25], v[20:21], s[88:89] op_sel_hi:[1,0]
	v_exp_f32_e32 v24, v24
	v_exp_f32_e32 v25, v25
	s_waitcnt lgkmcnt(0)
	global_store_dwordx2 v[18:19], v[22:23], off
	v_pk_fma_f32 v[18:19], v[88:89], s[38:39], v[8:9] op_sel_hi:[1,0,1]
	v_pk_fma_f32 v[28:29], v[82:83], s[38:39], v[6:7] op_sel_hi:[1,0,1]
	v_pk_add_f32 v[22:23], v[24:25], 1.0 op_sel_hi:[1,0]
	v_med3_f32 v19, v19, s55, v213
	v_rcp_f32_e32 v22, v22
	v_rcp_f32_e32 v23, v23
	v_med3_f32 v18, v18, s55, v213
	v_pk_add_f32 v[18:19], v[18:19], 1.0 op_sel_hi:[1,0]
	v_pk_fma_f32 v[24:25], v[90:91], s[38:39], v[10:11] op_sel_hi:[1,0,1]
	v_pk_mul_f32 v[18:19], v[20:21], v[18:19]
	v_pk_fma_f32 v[20:21], v[94:95], s[38:39], v[14:15] op_sel_hi:[1,0,1]
	v_pk_mul_f32 v[18:19], v[18:19], v[22:23]
	v_min_f32_e32 v21, 0x40e00000, v21
	v_min_f32_e32 v20, 0x40e00000, v20
	v_pk_mul_f32 v[22:23], v[20:21], s[88:89] op_sel_hi:[1,0]
	v_med3_f32 v25, v25, s55, v213
	v_med3_f32 v24, v24, s55, v213
	v_exp_f32_e32 v22, v22
	v_exp_f32_e32 v23, v23
	v_pk_add_f32 v[24:25], v[24:25], 1.0 op_sel_hi:[1,0]
	v_cvt_pk_fp8_f32 v30, v18, v19
	v_pk_mul_f32 v[20:21], v[20:21], v[24:25]
	v_pk_fma_f32 v[24:25], v[84:85], s[38:39], v[0:1] op_sel_hi:[1,0,1]
	v_pk_add_f32 v[22:23], v[22:23], 1.0 op_sel_hi:[1,0]
	v_min_f32_e32 v25, 0x40e00000, v25
	v_min_f32_e32 v24, 0x40e00000, v24
	v_pk_mul_f32 v[26:27], v[24:25], s[88:89] op_sel_hi:[1,0]
	v_rcp_f32_e32 v22, v22
	v_exp_f32_e32 v26, v26
	v_exp_f32_e32 v27, v27
	v_rcp_f32_e32 v23, v23
	v_med3_f32 v29, v29, s55, v213
	v_med3_f32 v28, v28, s55, v213
	v_pk_add_f32 v[26:27], v[26:27], 1.0 op_sel_hi:[1,0]
	v_pk_mul_f32 v[20:21], v[20:21], v[22:23]
	v_pk_fma_f32 v[22:23], v[80:81], s[38:39], v[4:5] op_sel_hi:[1,0,1]
	v_rcp_f32_e32 v26, v26
	v_rcp_f32_e32 v27, v27
	v_med3_f32 v23, v23, s55, v213
	v_med3_f32 v22, v22, s55, v213
	v_pk_add_f32 v[22:23], v[22:23], 1.0 op_sel_hi:[1,0]
	v_cvt_pk_fp8_f32 v30, v20, v21 op_sel:[0,0,1]
	v_pk_mul_f32 v[22:23], v[24:25], v[22:23]
	v_pk_fma_f32 v[20:21], v[76:77], s[38:39], v[12:13] op_sel_hi:[1,0,1]
	v_pk_mul_f32 v[22:23], v[22:23], v[26:27]
	v_pk_add_f32 v[18:19], v[28:29], 1.0 op_sel_hi:[1,0]
	v_min_f32_e32 v21, 0x40e00000, v21
	v_min_f32_e32 v20, 0x40e00000, v20
	v_pk_fma_f32 v[24:25], v[86:87], s[38:39], v[2:3] op_sel_hi:[1,0,1]
	v_cvt_pk_fp8_f32 v28, v22, v23
	v_pk_mul_f32 v[22:23], v[20:21], s[88:89] op_sel_hi:[1,0]
	v_min_f32_e32 v25, 0x40e00000, v25
	v_min_f32_e32 v24, 0x40e00000, v24
	v_exp_f32_e32 v22, v22
	v_exp_f32_e32 v23, v23
	v_pk_mul_f32 v[26:27], v[24:25], s[88:89] op_sel_hi:[1,0]
	v_pk_mul_f32 v[18:19], v[24:25], v[18:19]
	v_exp_f32_e32 v26, v26
	v_exp_f32_e32 v27, v27
	v_pk_add_f32 v[22:23], v[22:23], 1.0 op_sel_hi:[1,0]
	v_pk_fma_f32 v[24:25], v[72:73], s[38:39], v[8:9] op_sel_hi:[1,0,1]
	v_rcp_f32_e32 v22, v22
	v_rcp_f32_e32 v23, v23
	v_pk_add_f32 v[26:27], v[26:27], 1.0 op_sel_hi:[1,0]
	v_med3_f32 v25, v25, s55, v213
	v_med3_f32 v24, v24, s55, v213
	v_rcp_f32_e32 v26, v26
	v_rcp_f32_e32 v27, v27
	v_pk_add_f32 v[24:25], v[24:25], 1.0 op_sel_hi:[1,0]
	s_mov_b32 s0, 0x20000
	v_pk_mul_f32 v[20:21], v[20:21], v[24:25]
	v_pk_mul_f32 v[18:19], v[18:19], v[26:27]
	v_pk_mul_f32 v[20:21], v[20:21], v[22:23]
	v_pk_fma_f32 v[22:23], v[78:79], s[38:39], v[14:15] op_sel_hi:[1,0,1]
	v_pk_fma_f32 v[26:27], v[74:75], s[38:39], v[10:11] op_sel_hi:[1,0,1]
	v_min_f32_e32 v23, 0x40e00000, v23
	v_min_f32_e32 v22, 0x40e00000, v22
	v_pk_mul_f32 v[24:25], v[22:23], s[88:89] op_sel_hi:[1,0]
	v_cvt_pk_fp8_f32 v28, v18, v19 op_sel:[0,0,1]
	v_exp_f32_e32 v24, v24
	v_exp_f32_e32 v25, v25
	v_med3_f32 v27, v27, s55, v213
	v_med3_f32 v26, v26, s55, v213
	v_pk_add_f32 v[26:27], v[26:27], 1.0 op_sel_hi:[1,0]
	ds_bpermute_b32 v19, v167, v28
	v_pk_mul_f32 v[22:23], v[22:23], v[26:27]
	v_pk_fma_f32 v[26:27], v[68:69], s[38:39], v[0:1] op_sel_hi:[1,0,1]
	v_pk_add_f32 v[24:25], v[24:25], 1.0 op_sel_hi:[1,0]
	v_min_f32_e32 v27, 0x40e00000, v27
	v_min_f32_e32 v26, 0x40e00000, v26
	v_pk_mul_f32 v[28:29], v[26:27], s[88:89] op_sel_hi:[1,0]
	v_rcp_f32_e32 v24, v24
	v_rcp_f32_e32 v25, v25
	v_exp_f32_e32 v28, v28
	v_exp_f32_e32 v29, v29
	ds_bpermute_b32 v18, v167, v30
	v_pk_mul_f32 v[22:23], v[22:23], v[24:25]
	v_pk_fma_f32 v[24:25], v[64:65], s[38:39], v[4:5] op_sel_hi:[1,0,1]
	v_pk_add_f32 v[28:29], v[28:29], 1.0 op_sel_hi:[1,0]
	v_med3_f32 v25, v25, s55, v213
	v_rcp_f32_e32 v28, v28
	v_rcp_f32_e32 v29, v29
	v_med3_f32 v24, v24, s55, v213
	v_pk_add_f32 v[24:25], v[24:25], 1.0 op_sel_hi:[1,0]
	v_pk_fma_f32 v[30:31], v[66:67], s[38:39], v[6:7] op_sel_hi:[1,0,1]
	v_pk_mul_f32 v[24:25], v[26:27], v[24:25]
	v_pk_fma_f32 v[26:27], v[70:71], s[38:39], v[2:3] op_sel_hi:[1,0,1]
	v_pk_mul_f32 v[24:25], v[24:25], v[28:29]
	v_min_f32_e32 v27, 0x40e00000, v27
	v_min_f32_e32 v26, 0x40e00000, v26
	v_pk_mul_f32 v[28:29], v[26:27], s[88:89] op_sel_hi:[1,0]
	v_exp_f32_e32 v28, v28
	v_exp_f32_e32 v29, v29
	v_med3_f32 v31, v31, s55, v213
	v_med3_f32 v30, v30, s55, v213
	v_pk_add_f32 v[28:29], v[28:29], 1.0 op_sel_hi:[1,0]
	v_cvt_pk_fp8_f32 v64, v20, v21
	v_rcp_f32_e32 v28, v28
	v_rcp_f32_e32 v29, v29
	v_cvt_pk_fp8_f32 v65, v24, v25
	v_pk_add_f32 v[30:31], v[30:31], 1.0 op_sel_hi:[1,0]
	v_cvt_pk_fp8_f32 v64, v22, v23 op_sel:[0,0,1]
	v_pk_mul_f32 v[20:21], v[26:27], v[30:31]
	v_pk_fma_f32 v[22:23], v[60:61], s[38:39], v[12:13] op_sel_hi:[1,0,1]
	v_pk_mul_f32 v[20:21], v[20:21], v[28:29]
	v_min_f32_e32 v23, 0x40e00000, v23
	v_cvt_pk_fp8_f32 v65, v20, v21 op_sel:[0,0,1]
	v_add_co_u32_e32 v20, vcc, s0, v16
	v_min_f32_e32 v22, 0x40e00000, v22
	s_nop 0
	v_addc_co_u32_e32 v21, vcc, 0, v17, vcc
	s_waitcnt lgkmcnt(0)
	global_store_dwordx2 v[20:21], v[18:19], off
	ds_bpermute_b32 v18, v167, v64
	ds_bpermute_b32 v19, v167, v65
	v_pk_mul_f32 v[24:25], v[22:23], s[88:89] op_sel_hi:[1,0]
	s_mov_b32 s2, 0x24000
	v_exp_f32_e32 v24, v24
	v_exp_f32_e32 v25, v25
	v_add_co_u32_e32 v20, vcc, s2, v16
	s_nop 0
	v_addc_co_u32_e32 v21, vcc, 0, v17, vcc
	s_waitcnt lgkmcnt(0)
	global_store_dwordx2 v[20:21], v[18:19], off
	v_pk_add_f32 v[20:21], v[24:25], 1.0 op_sel_hi:[1,0]
	v_pk_fma_f32 v[18:19], v[56:57], s[38:39], v[8:9] op_sel_hi:[1,0,1]
	v_rcp_f32_e32 v20, v20
	v_rcp_f32_e32 v21, v21
	v_med3_f32 v19, v19, s55, v213
	v_med3_f32 v18, v18, s55, v213
	v_pk_add_f32 v[18:19], v[18:19], 1.0 op_sel_hi:[1,0]
	v_pk_fma_f32 v[24:25], v[58:59], s[38:39], v[10:11] op_sel_hi:[1,0,1]
	v_pk_mul_f32 v[18:19], v[22:23], v[18:19]
	v_med3_f32 v25, v25, s55, v213
	v_pk_mul_f32 v[18:19], v[18:19], v[20:21]
	v_pk_fma_f32 v[20:21], v[62:63], s[38:39], v[14:15] op_sel_hi:[1,0,1]
	v_med3_f32 v24, v24, s55, v213
	v_min_f32_e32 v21, 0x40e00000, v21
	v_min_f32_e32 v20, 0x40e00000, v20
	v_pk_mul_f32 v[22:23], v[20:21], s[88:89] op_sel_hi:[1,0]
	v_pk_add_f32 v[24:25], v[24:25], 1.0 op_sel_hi:[1,0]
	v_exp_f32_e32 v22, v22
	v_exp_f32_e32 v23, v23
	v_pk_mul_f32 v[20:21], v[20:21], v[24:25]
	v_pk_fma_f32 v[24:25], v[52:53], s[38:39], v[0:1] op_sel_hi:[1,0,1]
	v_cvt_pk_fp8_f32 v30, v18, v19
	v_min_f32_e32 v25, 0x40e00000, v25
	v_min_f32_e32 v24, 0x40e00000, v24
	v_pk_add_f32 v[22:23], v[22:23], 1.0 op_sel_hi:[1,0]
	v_pk_mul_f32 v[26:27], v[24:25], s[88:89] op_sel_hi:[1,0]
	v_rcp_f32_e32 v22, v22
	v_rcp_f32_e32 v23, v23
	v_exp_f32_e32 v26, v26
	v_exp_f32_e32 v27, v27
	v_pk_fma_f32 v[8:9], v[40:41], s[38:39], v[8:9] op_sel_hi:[1,0,1]
	v_pk_mul_f32 v[20:21], v[20:21], v[22:23]
	v_pk_fma_f32 v[22:23], v[48:49], s[38:39], v[4:5] op_sel_hi:[1,0,1]
	v_pk_add_f32 v[26:27], v[26:27], 1.0 op_sel_hi:[1,0]
	v_med3_f32 v23, v23, s55, v213
	v_rcp_f32_e32 v26, v26
	v_rcp_f32_e32 v27, v27
	v_med3_f32 v22, v22, s55, v213
	v_pk_fma_f32 v[12:13], v[44:45], s[38:39], v[12:13] op_sel_hi:[1,0,1]
	v_med3_f32 v9, v9, s55, v213
	v_med3_f32 v8, v8, s55, v213
	v_pk_add_f32 v[22:23], v[22:23], 1.0 op_sel_hi:[1,0]
	v_min_f32_e32 v13, 0x40e00000, v13
	v_min_f32_e32 v12, 0x40e00000, v12
	v_pk_add_f32 v[8:9], v[8:9], 1.0 op_sel_hi:[1,0]
	v_pk_fma_f32 v[10:11], v[42:43], s[38:39], v[10:11] op_sel_hi:[1,0,1]
	v_pk_mul_f32 v[22:23], v[24:25], v[22:23]
	v_pk_fma_f32 v[24:25], v[54:55], s[38:39], v[2:3] op_sel_hi:[1,0,1]
	v_cvt_pk_fp8_f32 v30, v20, v21 op_sel:[0,0,1]
	v_pk_mul_f32 v[20:21], v[12:13], s[88:89] op_sel_hi:[1,0]
	v_pk_mul_f32 v[8:9], v[12:13], v[8:9]
	v_pk_fma_f32 v[12:13], v[46:47], s[38:39], v[14:15] op_sel_hi:[1,0,1]
	v_med3_f32 v11, v11, s55, v213
	v_med3_f32 v10, v10, s55, v213
	v_pk_fma_f32 v[0:1], v[36:37], s[38:39], v[0:1] op_sel_hi:[1,0,1]
	v_min_f32_e32 v25, 0x40e00000, v25
	v_min_f32_e32 v24, 0x40e00000, v24
	v_min_f32_e32 v13, 0x40e00000, v13
	v_min_f32_e32 v12, 0x40e00000, v12
	v_pk_add_f32 v[10:11], v[10:11], 1.0 op_sel_hi:[1,0]
	v_min_f32_e32 v1, 0x40e00000, v1
	v_min_f32_e32 v0, 0x40e00000, v0
	v_pk_mul_f32 v[22:23], v[22:23], v[26:27]
	v_pk_mul_f32 v[26:27], v[24:25], s[88:89] op_sel_hi:[1,0]
	v_pk_mul_f32 v[14:15], v[12:13], s[88:89] op_sel_hi:[1,0]
	v_pk_mul_f32 v[10:11], v[12:13], v[10:11]
	v_pk_mul_f32 v[12:13], v[0:1], s[88:89] op_sel_hi:[1,0]
	v_exp_f32_e32 v26, v26
	v_exp_f32_e32 v27, v27
	v_exp_f32_e32 v20, v20
	v_exp_f32_e32 v21, v21
	v_exp_f32_e32 v12, v12
	v_exp_f32_e32 v13, v13
	v_pk_fma_f32 v[4:5], v[32:33], s[38:39], v[4:5] op_sel_hi:[1,0,1]
	v_pk_fma_f32 v[2:3], v[38:39], s[38:39], v[2:3] op_sel_hi:[1,0,1]
	v_med3_f32 v5, v5, s55, v213
	v_med3_f32 v4, v4, s55, v213
	v_pk_fma_f32 v[28:29], v[50:51], s[38:39], v[6:7] op_sel_hi:[1,0,1]
	v_pk_add_f32 v[4:5], v[4:5], 1.0 op_sel_hi:[1,0]
	v_min_f32_e32 v3, 0x40e00000, v3
	v_min_f32_e32 v2, 0x40e00000, v2
	v_med3_f32 v29, v29, s55, v213
	v_med3_f32 v28, v28, s55, v213
	v_pk_add_f32 v[26:27], v[26:27], 1.0 op_sel_hi:[1,0]
	v_pk_add_f32 v[20:21], v[20:21], 1.0 op_sel_hi:[1,0]
	v_pk_add_f32 v[12:13], v[12:13], 1.0 op_sel_hi:[1,0]
	v_pk_mul_f32 v[0:1], v[0:1], v[4:5]
	v_pk_mul_f32 v[4:5], v[2:3], s[88:89] op_sel_hi:[1,0]
	v_rcp_f32_e32 v26, v26
	v_rcp_f32_e32 v27, v27
	v_pk_add_f32 v[18:19], v[28:29], 1.0 op_sel_hi:[1,0]
	v_rcp_f32_e32 v20, v20
	v_rcp_f32_e32 v21, v21
	v_exp_f32_e32 v14, v14
	v_exp_f32_e32 v15, v15
	v_rcp_f32_e32 v12, v12
	v_rcp_f32_e32 v13, v13
	v_exp_f32_e32 v4, v4
	v_exp_f32_e32 v5, v5
	v_cvt_pk_fp8_f32 v28, v22, v23
	v_pk_mul_f32 v[18:19], v[24:25], v[18:19]
	v_pk_mul_f32 v[8:9], v[8:9], v[20:21]
	v_pk_mul_f32 v[18:19], v[18:19], v[26:27]
	v_pk_add_f32 v[14:15], v[14:15], 1.0 op_sel_hi:[1,0]
	v_pk_mul_f32 v[0:1], v[0:1], v[12:13]
	v_pk_add_f32 v[4:5], v[4:5], 1.0 op_sel_hi:[1,0]
	v_cvt_pk_fp8_f32 v28, v18, v19 op_sel:[0,0,1]
	v_rcp_f32_e32 v14, v14
	v_rcp_f32_e32 v15, v15
	v_pk_fma_f32 v[6:7], v[34:35], s[38:39], v[6:7] op_sel_hi:[1,0,1]
	v_rcp_f32_e32 v4, v4
	v_rcp_f32_e32 v5, v5
	v_cvt_pk_fp8_f32 v12, v8, v9
	v_med3_f32 v7, v7, s55, v213
	v_med3_f32 v6, v6, s55, v213
	v_cvt_pk_fp8_f32 v8, v0, v1
	v_pk_add_f32 v[6:7], v[6:7], 1.0 op_sel_hi:[1,0]
	ds_bpermute_b32 v18, v167, v30
	v_pk_mul_f32 v[0:1], v[2:3], v[6:7]
	ds_bpermute_b32 v19, v167, v28
	v_pk_mul_f32 v[10:11], v[10:11], v[14:15]
	v_pk_mul_f32 v[0:1], v[0:1], v[4:5]
	v_cvt_pk_fp8_f32 v12, v10, v11 op_sel:[0,0,1]
	v_cvt_pk_fp8_f32 v8, v0, v1 op_sel:[0,0,1]
	s_mov_b32 s2, 0x28000
	v_add_co_u32_e32 v0, vcc, s2, v16
	v_mov_b32_e32 v174, v218
	s_nop 0
	v_addc_co_u32_e32 v1, vcc, 0, v17, vcc
	s_waitcnt lgkmcnt(0)
	global_store_dwordx2 v[0:1], v[18:19], off
	ds_bpermute_b32 v0, v167, v12
	ds_bpermute_b32 v1, v167, v8
	v_add_co_u32_e32 v2, vcc, 0x2c000, v16
	v_mov_b32_e32 v168, v216
	s_nop 0
	v_addc_co_u32_e32 v3, vcc, 0, v17, vcc
	s_and_b64 vcc, exec, s[14:15]
	v_mov_b32_e32 v170, v217
	v_mov_b32_e32 v166, v215
	v_mov_b32_e32 v219, v197
	v_mov_b32_e32 v220, v196
	s_mov_b64 s[24:25], s[16:17]
	s_mov_b64 s[22:23], s[18:19]
	s_mov_b32 s57, s1
	v_readlane_b32 s64, v255, 32
	s_movk_i32 s72, 0x48
	s_waitcnt lgkmcnt(0)
	global_store_dwordx2 v[2:3], v[0:1], off
	s_cbranch_vccnz .LBB0_1563

.LBB0_1655:
	s_mul_hi_u32 s7, s82, 0xaaaaaaab
	s_lshr_b32 s7, s7, 1
	s_mul_i32 s7, s7, 3
	s_sub_i32 s7, s82, s7
	s_nop 15
	s_nop 15
	v_lshl_add_u32 v30, s7, 10, v175
	ds_read_b128 v[4:7], v30
	ds_read_b128 v[8:11], v30 offset:16
	s_mov_b32 s0, 0x41000000
	v_lshl_or_b32 v2, s14, 8, v194
	s_waitcnt lgkmcnt(0)
	v_pk_mul_f32 v[20:21], v[4:5], s[0:1] op_sel_hi:[1,0]
	v_pk_mul_f32 v[22:23], v[8:9], s[0:1] op_sel_hi:[1,0]
	v_pk_mul_f32 v[18:19], v[6:7], s[0:1] op_sel_hi:[1,0]
	v_pk_fma_f32 v[0:1], v[156:157], s[74:75], v[20:21] op_sel_hi:[1,0,1]
	v_pk_fma_f32 v[4:5], v[152:153], s[74:75], v[22:23] op_sel_hi:[1,0,1]
	v_cvt_pk_fp8_f32 v6, v0, v1
	v_cvt_pk_fp8_f32 v7, v4, v5
	v_pk_mul_f32 v[24:25], v[10:11], s[0:1] op_sel_hi:[1,0]
	v_pk_fma_f32 v[0:1], v[158:159], s[74:75], v[18:19] op_sel_hi:[1,0,1]
	v_pk_fma_f32 v[4:5], v[154:155], s[74:75], v[24:25] op_sel_hi:[1,0,1]
	v_cvt_pk_fp8_f32 v6, v0, v1 op_sel:[0,0,1]
	v_cvt_pk_fp8_f32 v7, v4, v5 op_sel:[0,0,1]
	v_lshl_add_u32 v8, s12, 8, v193
	v_ashrrev_i32_e32 v9, 31, v8
	ds_bpermute_b32 v0, v169, v6
	ds_bpermute_b32 v1, v169, v7
	v_lshlrev_b64 v[4:5], 10, v[8:9]
	v_pk_fma_f32 v[6:7], v[148:149], s[74:75], v[20:21] op_sel_hi:[1,0,1]
	v_cvt_pk_fp8_f32 v9, v6, v7
	v_pk_fma_f32 v[10:11], v[144:145], s[74:75], v[22:23] op_sel_hi:[1,0,1]
	v_pk_fma_f32 v[6:7], v[150:151], s[74:75], v[18:19] op_sel_hi:[1,0,1]
	v_cvt_pk_fp8_f32 v12, v10, v11
	v_cvt_pk_fp8_f32 v9, v6, v7 op_sel:[0,0,1]
	v_ashrrev_i32_e32 v3, 31, v2
	v_lshl_add_u64 v[4:5], s[68:69], 0, v[4:5]
	v_pk_fma_f32 v[10:11], v[146:147], s[74:75], v[24:25] op_sel_hi:[1,0,1]
	v_lshl_add_u64 v[14:15], v[4:5], 0, v[2:3]
	v_cvt_pk_fp8_f32 v12, v10, v11 op_sel:[0,0,1]
	s_waitcnt lgkmcnt(0)
	global_store_dwordx2 v[14:15], v[0:1], off
	ds_bpermute_b32 v0, v169, v9
	v_pk_fma_f32 v[6:7], v[140:141], s[74:75], v[20:21] op_sel_hi:[1,0,1]
	v_cvt_pk_fp8_f32 v9, v6, v7
	ds_bpermute_b32 v1, v169, v12
	v_or_b32_e32 v4, 16, v8
	v_pk_fma_f32 v[10:11], v[136:137], s[74:75], v[22:23] op_sel_hi:[1,0,1]
	v_pk_fma_f32 v[6:7], v[142:143], s[74:75], v[18:19] op_sel_hi:[1,0,1]
	v_ashrrev_i32_e32 v5, 31, v4
	v_cvt_pk_fp8_f32 v12, v10, v11
	v_cvt_pk_fp8_f32 v9, v6, v7 op_sel:[0,0,1]
	v_lshlrev_b64 v[4:5], 10, v[4:5]
	v_lshl_add_u64 v[4:5], s[68:69], 0, v[4:5]
	v_pk_fma_f32 v[10:11], v[138:139], s[74:75], v[24:25] op_sel_hi:[1,0,1]
	v_lshl_add_u64 v[6:7], v[4:5], 0, v[2:3]
	v_cvt_pk_fp8_f32 v12, v10, v11 op_sel:[0,0,1]
	s_waitcnt lgkmcnt(0)
	global_store_dwordx2 v[6:7], v[0:1], off
	ds_bpermute_b32 v0, v169, v9
	v_pk_fma_f32 v[10:11], v[132:133], s[74:75], v[20:21] op_sel_hi:[1,0,1]
	v_cvt_pk_fp8_f32 v9, v10, v11
	ds_bpermute_b32 v1, v169, v12
	v_pk_fma_f32 v[12:13], v[128:129], s[74:75], v[22:23] op_sel_hi:[1,0,1]
	v_pk_fma_f32 v[10:11], v[134:135], s[74:75], v[18:19] op_sel_hi:[1,0,1]
	v_or_b32_e32 v4, 32, v8
	v_cvt_pk_fp8_f32 v16, v12, v13
	v_cvt_pk_fp8_f32 v9, v10, v11 op_sel:[0,0,1]
	v_ashrrev_i32_e32 v5, 31, v4
	v_lshlrev_b64 v[4:5], 10, v[4:5]
	v_lshl_add_u64 v[4:5], s[68:69], 0, v[4:5]
	v_pk_fma_f32 v[12:13], v[130:131], s[74:75], v[24:25] op_sel_hi:[1,0,1]
	v_pk_fma_f32 v[10:11], v[124:125], s[74:75], v[20:21] op_sel_hi:[1,0,1]
	v_cvt_pk_fp8_f32 v16, v12, v13 op_sel:[0,0,1]
	v_lshl_add_u64 v[12:13], v[4:5], 0, v[2:3]
	ds_bpermute_b32 v4, v169, v9
	v_cvt_pk_fp8_f32 v9, v10, v11
	ds_bpermute_b32 v5, v169, v16
	v_pk_fma_f32 v[16:17], v[120:121], s[74:75], v[22:23] op_sel_hi:[1,0,1]
	v_pk_fma_f32 v[10:11], v[126:127], s[74:75], v[18:19] op_sel_hi:[1,0,1]
	v_cvt_pk_fp8_f32 v26, v16, v17
	v_cvt_pk_fp8_f32 v9, v10, v11 op_sel:[0,0,1]
	v_pk_fma_f32 v[16:17], v[122:123], s[74:75], v[24:25] op_sel_hi:[1,0,1]
	v_cvt_pk_fp8_f32 v26, v16, v17 op_sel:[0,0,1]
	ds_bpermute_b32 v10, v169, v9
	v_pk_fma_f32 v[16:17], v[116:117], s[74:75], v[20:21] op_sel_hi:[1,0,1]
	v_cvt_pk_fp8_f32 v9, v16, v17
	ds_bpermute_b32 v11, v169, v26
	v_pk_fma_f32 v[26:27], v[112:113], s[74:75], v[22:23] op_sel_hi:[1,0,1]
	v_pk_fma_f32 v[16:17], v[118:119], s[74:75], v[18:19] op_sel_hi:[1,0,1]
	v_cvt_pk_fp8_f32 v28, v26, v27
	v_cvt_pk_fp8_f32 v9, v16, v17 op_sel:[0,0,1]
	v_pk_fma_f32 v[26:27], v[114:115], s[74:75], v[24:25] op_sel_hi:[1,0,1]
	s_waitcnt lgkmcnt(0)
	global_store_dwordx2 v[12:13], v[0:1], off
	v_or_b32_e32 v0, 48, v8
	v_cvt_pk_fp8_f32 v28, v26, v27 op_sel:[0,0,1]
	ds_bpermute_b32 v16, v169, v9
	v_pk_fma_f32 v[26:27], v[108:109], s[74:75], v[20:21] op_sel_hi:[1,0,1]
	v_ashrrev_i32_e32 v1, 31, v0
	v_cvt_pk_fp8_f32 v9, v26, v27
	v_lshlrev_b64 v[0:1], 10, v[0:1]
	v_lshl_add_u64 v[0:1], s[68:69], 0, v[0:1]
	v_lshl_add_u64 v[0:1], v[0:1], 0, v[2:3]
	ds_bpermute_b32 v17, v169, v28
	v_pk_fma_f32 v[28:29], v[104:105], s[74:75], v[22:23] op_sel_hi:[1,0,1]
	v_pk_fma_f32 v[26:27], v[110:111], s[74:75], v[18:19] op_sel_hi:[1,0,1]
	global_store_dwordx2 v[0:1], v[4:5], off
	v_add_u32_e32 v4, 0x80, v8
	v_cvt_pk_fp8_f32 v31, v28, v29
	v_cvt_pk_fp8_f32 v9, v26, v27 op_sel:[0,0,1]
	v_ashrrev_i32_e32 v5, 31, v4
	v_lshlrev_b64 v[4:5], 10, v[4:5]
	v_lshl_add_u64 v[4:5], s[68:69], 0, v[4:5]
	v_pk_fma_f32 v[28:29], v[106:107], s[74:75], v[24:25] op_sel_hi:[1,0,1]
	v_lshl_add_u64 v[4:5], v[4:5], 0, v[2:3]
	v_cvt_pk_fp8_f32 v31, v28, v29 op_sel:[0,0,1]
	ds_bpermute_b32 v26, v169, v9
	v_pk_fma_f32 v[20:21], v[92:93], s[74:75], v[20:21] op_sel_hi:[1,0,1]
	v_pk_fma_f32 v[22:23], v[88:89], s[74:75], v[22:23] op_sel_hi:[1,0,1]
	global_store_dwordx2 v[4:5], v[10:11], off
	v_add_u32_e32 v10, 0x90, v8
	v_cvt_pk_fp8_f32 v9, v20, v21
	v_cvt_pk_fp8_f32 v28, v22, v23
	v_ashrrev_i32_e32 v11, 31, v10
	v_lshlrev_b64 v[10:11], 10, v[10:11]
	v_lshl_add_u64 v[10:11], s[68:69], 0, v[10:11]
	v_pk_fma_f32 v[18:19], v[94:95], s[74:75], v[18:19] op_sel_hi:[1,0,1]
	v_pk_fma_f32 v[20:21], v[90:91], s[74:75], v[24:25] op_sel_hi:[1,0,1]
	v_lshl_add_u64 v[10:11], v[10:11], 0, v[2:3]
	v_cvt_pk_fp8_f32 v9, v18, v19 op_sel:[0,0,1]
	v_cvt_pk_fp8_f32 v28, v20, v21 op_sel:[0,0,1]
	ds_read_b128 v[18:21], v30 offset:512
	ds_read_b128 v[22:25], v30 offset:528
	s_waitcnt lgkmcnt(0)
	global_store_dwordx2 v[10:11], v[16:17], off
	ds_bpermute_b32 v27, v169, v31
	v_add_u32_e32 v16, 0xa0, v8
	v_ashrrev_i32_e32 v17, 31, v16
	v_lshlrev_b64 v[16:17], 10, v[16:17]
	v_lshl_add_u64 v[16:17], s[68:69], 0, v[16:17]
	v_lshl_add_u64 v[16:17], v[16:17], 0, v[2:3]
	v_pk_mul_f32 v[18:19], v[18:19], s[0:1] op_sel_hi:[1,0]
	v_pk_mul_f32 v[22:23], v[22:23], s[0:1] op_sel_hi:[1,0]
	s_waitcnt lgkmcnt(0)
	global_store_dwordx2 v[16:17], v[26:27], off
	ds_bpermute_b32 v27, v169, v28
	v_pk_fma_f32 v[28:29], v[100:101], s[74:75], v[18:19] op_sel_hi:[1,0,1]
	v_pk_fma_f32 v[30:31], v[96:97], s[74:75], v[22:23] op_sel_hi:[1,0,1]
	v_cvt_pk_fp8_f32 v88, v28, v29
	v_cvt_pk_fp8_f32 v89, v30, v31
	v_pk_mul_f32 v[20:21], v[20:21], s[0:1] op_sel_hi:[1,0]
	v_pk_mul_f32 v[24:25], v[24:25], s[0:1] op_sel_hi:[1,0]
	v_pk_fma_f32 v[28:29], v[102:103], s[74:75], v[20:21] op_sel_hi:[1,0,1]
	v_pk_fma_f32 v[30:31], v[98:99], s[74:75], v[24:25] op_sel_hi:[1,0,1]
	v_cvt_pk_fp8_f32 v88, v28, v29 op_sel:[0,0,1]
	v_cvt_pk_fp8_f32 v89, v30, v31 op_sel:[0,0,1]
	ds_bpermute_b32 v26, v169, v9
	v_add_u32_e32 v8, 0xb0, v8
	v_ashrrev_i32_e32 v9, 31, v8
	ds_bpermute_b32 v28, v169, v88
	ds_bpermute_b32 v29, v169, v89
	v_lshlrev_b64 v[8:9], 10, v[8:9]
	v_lshl_add_u64 v[8:9], s[68:69], 0, v[8:9]
	v_lshl_add_u64 v[2:3], v[8:9], 0, v[2:3]
	s_waitcnt lgkmcnt(0)
	global_store_dwordx2 v[2:3], v[26:27], off
	global_store_dwordx2 v[14:15], v[28:29], off offset:128
	v_pk_fma_f32 v[8:9], v[84:85], s[74:75], v[18:19] op_sel_hi:[1,0,1]
	v_pk_fma_f32 v[14:15], v[80:81], s[74:75], v[22:23] op_sel_hi:[1,0,1]
	v_cvt_pk_fp8_f32 v26, v8, v9
	v_cvt_pk_fp8_f32 v27, v14, v15
	v_pk_fma_f32 v[8:9], v[86:87], s[74:75], v[20:21] op_sel_hi:[1,0,1]
	v_pk_fma_f32 v[14:15], v[82:83], s[74:75], v[24:25] op_sel_hi:[1,0,1]
	v_cvt_pk_fp8_f32 v26, v8, v9 op_sel:[0,0,1]
	v_cvt_pk_fp8_f32 v27, v14, v15 op_sel:[0,0,1]
	v_pk_fma_f32 v[8:9], v[76:77], s[74:75], v[18:19] op_sel_hi:[1,0,1]
	v_pk_fma_f32 v[14:15], v[72:73], s[74:75], v[22:23] op_sel_hi:[1,0,1]
	v_cvt_pk_fp8_f32 v28, v8, v9
	v_cvt_pk_fp8_f32 v29, v14, v15
	v_pk_fma_f32 v[8:9], v[78:79], s[74:75], v[20:21] op_sel_hi:[1,0,1]
	v_pk_fma_f32 v[14:15], v[74:75], s[74:75], v[24:25] op_sel_hi:[1,0,1]
	v_cvt_pk_fp8_f32 v28, v8, v9 op_sel:[0,0,1]
	v_cvt_pk_fp8_f32 v29, v14, v15 op_sel:[0,0,1]
	ds_bpermute_b32 v8, v169, v26
	ds_bpermute_b32 v9, v169, v27
	ds_bpermute_b32 v14, v169, v28
	ds_bpermute_b32 v15, v169, v29
	v_pk_fma_f32 v[26:27], v[68:69], s[74:75], v[18:19] op_sel_hi:[1,0,1]
	s_waitcnt lgkmcnt(0)
	global_store_dwordx2 v[6:7], v[8:9], off offset:128
	global_store_dwordx2 v[12:13], v[14:15], off offset:128
	v_pk_fma_f32 v[8:9], v[60:61], s[74:75], v[18:19] op_sel_hi:[1,0,1]
	v_pk_fma_f32 v[12:13], v[56:57], s[74:75], v[22:23] op_sel_hi:[1,0,1]
	v_cvt_pk_fp8_f32 v30, v26, v27
	v_cvt_pk_fp8_f32 v14, v8, v9
	v_cvt_pk_fp8_f32 v15, v12, v13
	v_pk_fma_f32 v[26:27], v[70:71], s[74:75], v[20:21] op_sel_hi:[1,0,1]
	v_pk_fma_f32 v[8:9], v[62:63], s[74:75], v[20:21] op_sel_hi:[1,0,1]
	v_pk_fma_f32 v[12:13], v[58:59], s[74:75], v[24:25] op_sel_hi:[1,0,1]
	v_pk_fma_f32 v[28:29], v[64:65], s[74:75], v[22:23] op_sel_hi:[1,0,1]
	v_cvt_pk_fp8_f32 v30, v26, v27 op_sel:[0,0,1]
	v_cvt_pk_fp8_f32 v14, v8, v9 op_sel:[0,0,1]
	v_cvt_pk_fp8_f32 v15, v12, v13 op_sel:[0,0,1]
	v_pk_fma_f32 v[8:9], v[52:53], s[74:75], v[18:19] op_sel_hi:[1,0,1]
	v_pk_fma_f32 v[12:13], v[48:49], s[74:75], v[22:23] op_sel_hi:[1,0,1]
	v_cvt_pk_fp8_f32 v31, v28, v29
	v_cvt_pk_fp8_f32 v26, v8, v9
	v_cvt_pk_fp8_f32 v27, v12, v13
	v_pk_fma_f32 v[28:29], v[66:67], s[74:75], v[24:25] op_sel_hi:[1,0,1]
	v_pk_fma_f32 v[8:9], v[54:55], s[74:75], v[20:21] op_sel_hi:[1,0,1]
	v_pk_fma_f32 v[12:13], v[50:51], s[74:75], v[24:25] op_sel_hi:[1,0,1]
	v_cvt_pk_fp8_f32 v31, v28, v29 op_sel:[0,0,1]
	v_cvt_pk_fp8_f32 v26, v8, v9 op_sel:[0,0,1]
	v_cvt_pk_fp8_f32 v27, v12, v13 op_sel:[0,0,1]
	ds_bpermute_b32 v8, v169, v14
	ds_bpermute_b32 v9, v169, v15
	v_pk_fma_f32 v[14:15], v[44:45], s[74:75], v[18:19] op_sel_hi:[1,0,1]
	v_cvt_pk_fp8_f32 v28, v14, v15
	ds_bpermute_b32 v12, v169, v26
	ds_bpermute_b32 v13, v169, v27
	v_pk_fma_f32 v[26:27], v[40:41], s[74:75], v[22:23] op_sel_hi:[1,0,1]
	v_pk_fma_f32 v[14:15], v[46:47], s[74:75], v[20:21] op_sel_hi:[1,0,1]
	v_cvt_pk_fp8_f32 v29, v26, v27
	v_cvt_pk_fp8_f32 v28, v14, v15 op_sel:[0,0,1]
	v_pk_fma_f32 v[14:15], v[36:37], s[74:75], v[18:19] op_sel_hi:[1,0,1]
	v_pk_fma_f32 v[18:19], v[32:33], s[74:75], v[22:23] op_sel_hi:[1,0,1]
	v_cvt_pk_fp8_f32 v22, v14, v15
	v_cvt_pk_fp8_f32 v23, v18, v19
	v_pk_fma_f32 v[26:27], v[42:43], s[74:75], v[24:25] op_sel_hi:[1,0,1]
	v_pk_fma_f32 v[14:15], v[38:39], s[74:75], v[20:21] op_sel_hi:[1,0,1]
	v_cvt_pk_fp8_f32 v29, v26, v27 op_sel:[0,0,1]
	v_pk_fma_f32 v[18:19], v[34:35], s[74:75], v[24:25] op_sel_hi:[1,0,1]
	ds_bpermute_b32 v6, v169, v30
	ds_bpermute_b32 v7, v169, v31
	v_cvt_pk_fp8_f32 v22, v14, v15 op_sel:[0,0,1]
	v_cvt_pk_fp8_f32 v23, v18, v19 op_sel:[0,0,1]
	ds_bpermute_b32 v14, v169, v28
	ds_bpermute_b32 v15, v169, v29
	v_readlane_b32 s90, v255, 27
	ds_bpermute_b32 v18, v169, v22
	ds_bpermute_b32 v19, v169, v23
	s_and_b64 vcc, exec, s[20:21]
	v_mov_b32_e32 v170, v214
	v_mov_b32_e32 v166, v196
	v_mov_b32_e32 v174, v197
	v_mov_b32_e32 v168, v195
	s_mov_b32 s12, s81
	s_mov_b32 s14, s80
	s_mov_b64 s[24:25], s[16:17]
	s_mov_b64 s[22:23], s[18:19]
	s_mov_b32 s82, s73
	v_readlane_b32 s91, v255, 28
	v_readlane_b32 s73, v255, 29
	v_readlane_b32 s87, v255, 30
	v_readlane_b32 s85, v255, 31
	s_waitcnt lgkmcnt(0)
	global_store_dwordx2 v[0:1], v[6:7], off offset:128
	global_store_dwordx2 v[4:5], v[8:9], off offset:128
	global_store_dwordx2 v[10:11], v[12:13], off offset:128
	global_store_dwordx2 v[16:17], v[14:15], off offset:128
	global_store_dwordx2 v[2:3], v[18:19], off offset:128
	s_cbranch_vccnz .LBB0_1672
